# baseline (speedup 1.0000x reference)
.LBB7_3:
	s_ff1_i32_b32 s44, s21
	s_lshr_b32 s45, s23, s44
	s_lshl_b32 s46, s45, 7
	s_mul_i32 s47, s45, s21
	s_sub_i32 s47, s23, s47
	s_lshl_b32 s48, s47, 7
	s_ashr_i32 s49, s48, 31
	v_or_b32_e32 v152, s46, v1
	v_lshl_add_u64 v[154:155], s[48:49], 1, v[70:71]
	v_mad_i64_i32 v[156:157], s[50:51], v152, s29, v[154:155]
	v_lshl_add_u64 v[158:159], s[48:49], 2, v[68:69]
	v_or_b32_e32 v153, 32, v152
	global_load_dwordx4 v[160:163], v[156:157], off
	v_mad_i64_i32 v[184:185], s[50:51], v153, s29, v[154:155]
	v_or_b32_e32 v153, 64, v152
	global_load_dwordx4 v[176:179], v[158:159], off
	global_load_dwordx4 v[180:183], v[158:159], off offset:16
	v_mad_i64_i32 v[186:187], s[50:51], v153, s29, v[154:155]
	v_or_b32_e32 v153, 0x60, v152
	global_load_dwordx4 v[164:167], v[184:185], off
	v_mad_i64_i32 v[188:189], s[50:51], v153, s29, v[154:155]
	global_load_dwordx4 v[168:171], v[186:187], off
	s_nop 0
	global_load_dwordx4 v[172:175], v[188:189], off
	v_add_u32_e32 v67, v80, v77
	s_waitcnt vmcnt(14)
	s_barrier
	s_waitcnt lgkmcnt(0)
	ds_read_b128 v[2:5], v67 offset:16384
	v_add_u32_e32 v109, v79, v77
	ds_read_b128 v[6:9], v109
	ds_read_b128 v[10:13], v109 offset:4096
	ds_read_b128 v[14:17], v67 offset:20480
	v_add_u32_e32 v126, v80, v76
	ds_read_b128 v[34:37], v126 offset:16384
	v_add_u32_e32 v127, v79, v76
	s_waitcnt lgkmcnt(3)
	v_mfma_f32_32x32x16_f16 v[50:65], v[2:5], v[6:9], 0
	ds_read_b128 v[110:113], v127
	ds_read_b128 v[114:117], v127 offset:4096
	ds_read_b128 v[118:121], v126 offset:20480
	v_readfirstlane_b32 s2, v0
	s_lshl_b32 s19, s27, 15
	s_lshl_b32 s2, s2, 4
	s_add_i32 s1, s19, 0
	s_and_b32 s31, s2, 0xfffffc00
	s_add_i32 s1, s1, s31
	s_waitcnt lgkmcnt(5)
	v_mfma_f32_32x32x16_f16 v[18:33], v[2:5], v[10:13], 0
	s_mov_b32 m0, s1
	s_add_i32 s2, s1, 0x2000
	buffer_load_dwordx4 v72, s[4:7], s0 offen lds
	s_mov_b32 m0, s2
	s_add_i32 s3, s1, 0x4000
	buffer_load_dwordx4 v74, s[4:7], s0 offen lds
	s_mov_b32 s14, s10
	s_waitcnt lgkmcnt(2)
	v_mfma_f32_32x32x16_f16 v[50:65], v[34:37], v[110:113], v[50:65]
	s_mov_b32 s15, s11
	s_mov_b32 m0, s3
	s_add_i32 s18, s1, 0x6000
	buffer_load_dwordx4 v73, s[12:15], s0 offen lds
	s_mov_b32 m0, s18
	s_add_i32 s33, s19, 0x8000
	buffer_load_dwordx4 v75, s[12:15], s0 offen lds
	s_waitcnt lgkmcnt(1)
	v_mfma_f32_32x32x16_f16 v[18:33], v[34:37], v[114:117], v[18:33]
	s_waitcnt vmcnt(14)
	s_barrier
	s_and_b32 s33, s33, 0x18000
	s_add_i32 s33, s33, 0
	s_add_i32 s33, s33, s31
	s_add_i32 s34, s0, 0x80
	s_mov_b32 m0, s33
	v_mfma_f32_32x32x16_f16 v[34:49], v[14:17], v[6:9], 0
	v_add_u32_e32 v128, v81, v77
	v_add_u32_e32 v129, v82, v77
	v_add_u32_e32 v130, v81, v76
	v_add_u32_e32 v131, v82, v76
	s_xor_b32 s19, s19, 0x10000
	v_add_u32_e32 v134, v83, v77
	v_add_u32_e32 v138, v84, v77
	v_mfma_f32_32x32x16_f16 v[2:17], v[14:17], v[10:13], 0
	v_add_u32_e32 v142, v83, v76
	v_add_u32_e32 v146, v84, v76
	s_waitcnt lgkmcnt(0)
	v_mfma_f32_32x32x16_f16 v[34:49], v[118:121], v[110:113], v[34:49]
	v_mfma_f32_32x32x16_f16 v[2:17], v[118:121], v[114:117], v[2:17]
	ds_read_b128 v[110:113], v67 offset:49152
	ds_read_b128 v[114:117], v109 offset:32768
	ds_read_b128 v[118:121], v109 offset:36864
	ds_read_b128 v[122:125], v67 offset:53248
	s_waitcnt lgkmcnt(2)
	v_mfma_f32_32x32x16_f16 v[50:65], v[110:113], v[114:117], v[50:65]
	s_waitcnt lgkmcnt(1)
	v_mfma_f32_32x32x16_f16 v[18:33], v[110:113], v[118:121], v[18:33]
	s_waitcnt lgkmcnt(0)
	v_mfma_f32_32x32x16_f16 v[34:49], v[122:125], v[114:117], v[34:49]
	v_mfma_f32_32x32x16_f16 v[2:17], v[122:125], v[118:121], v[2:17]
	ds_read_b128 v[110:113], v126 offset:49152
	ds_read_b128 v[114:117], v127 offset:32768
	ds_read_b128 v[118:121], v127 offset:36864
	ds_read_b128 v[122:125], v126 offset:53248
	buffer_load_dwordx4 v72, s[4:7], s34 offen lds
	s_add_i32 m0, s33, 0x2000
	s_nop 0
	buffer_load_dwordx4 v74, s[4:7], s34 offen lds
	s_add_i32 m0, s33, 0x4000
	s_nop 0
	buffer_load_dwordx4 v73, s[12:15], s34 offen lds
	s_add_i32 m0, s33, 0x6000
	s_waitcnt lgkmcnt(2)
	v_mfma_f32_32x32x16_f16 v[50:65], v[110:113], v[114:117], v[50:65]
	buffer_load_dwordx4 v75, s[12:15], s34 offen lds
	s_waitcnt vmcnt(14)
	s_barrier
	s_add_i32 s33, s19, 0
	s_add_i32 s33, s33, s31
	s_add_i32 s34, s0, 0x100
	s_mov_b32 m0, s33
	s_waitcnt lgkmcnt(1)
	v_mfma_f32_32x32x16_f16 v[18:33], v[110:113], v[118:121], v[18:33]
	ds_read_b128 v[110:113], v96
	s_add_i32 s19, s19, 0x8000
	s_and_b32 s19, s19, 0x18000
	s_add_i32 s19, s19, 0
	s_add_i32 s19, s19, s31
	s_add_i32 s31, s0, 0x180
	s_waitcnt lgkmcnt(1)
	v_mfma_f32_32x32x16_f16 v[34:49], v[122:125], v[114:117], v[34:49]
	v_mfma_f32_32x32x16_f16 v[2:17], v[122:125], v[118:121], v[2:17]
	ds_read_b128 v[114:117], v128
	ds_read_b128 v[118:121], v128 offset:4096
	ds_read_b128 v[122:125], v129 offset:4096
	s_waitcnt lgkmcnt(2)
	v_mfma_f32_32x32x16_f16 v[50:65], v[110:113], v[114:117], v[50:65]
	s_waitcnt lgkmcnt(1)
	v_mfma_f32_32x32x16_f16 v[18:33], v[110:113], v[118:121], v[18:33]
	ds_read_b128 v[110:113], v97
	s_waitcnt lgkmcnt(1)
	v_mfma_f32_32x32x16_f16 v[34:49], v[122:125], v[114:117], v[34:49]
	v_mfma_f32_32x32x16_f16 v[2:17], v[122:125], v[118:121], v[2:17]
	ds_read_b128 v[114:117], v130
	ds_read_b128 v[118:121], v130 offset:4096
	ds_read_b128 v[122:125], v131 offset:4096
	buffer_load_dwordx4 v72, s[4:7], s34 offen lds
	s_add_i32 m0, s33, 0x2000
	s_nop 0
	buffer_load_dwordx4 v74, s[4:7], s34 offen lds
	s_add_i32 m0, s33, 0x4000
	s_waitcnt lgkmcnt(2)
	v_mfma_f32_32x32x16_f16 v[50:65], v[110:113], v[114:117], v[50:65]
	buffer_load_dwordx4 v73, s[12:15], s34 offen lds
	s_add_i32 m0, s33, 0x6000
	s_nop 0
	buffer_load_dwordx4 v75, s[12:15], s34 offen lds
	s_waitcnt vmcnt(8)
	s_barrier
	s_mov_b32 m0, s19
	s_waitcnt lgkmcnt(1)
	v_mfma_f32_32x32x16_f16 v[18:33], v[110:113], v[118:121], v[18:33]
	ds_read_b128 v[110:113], v98
	s_waitcnt lgkmcnt(1)
	v_mfma_f32_32x32x16_f16 v[34:49], v[122:125], v[114:117], v[34:49]
	v_mfma_f32_32x32x16_f16 v[2:17], v[122:125], v[118:121], v[2:17]
	ds_read_b128 v[114:117], v134
	ds_read_b128 v[118:121], v134 offset:4096
	ds_read_b128 v[122:125], v138 offset:4096
	s_waitcnt lgkmcnt(2)
	v_mfma_f32_32x32x16_f16 v[50:65], v[110:113], v[114:117], v[50:65]
	s_waitcnt lgkmcnt(1)
	v_mfma_f32_32x32x16_f16 v[18:33], v[110:113], v[118:121], v[18:33]
	ds_read_b128 v[110:113], v99
	s_waitcnt lgkmcnt(1)
	v_mfma_f32_32x32x16_f16 v[34:49], v[122:125], v[114:117], v[34:49]
	v_mfma_f32_32x32x16_f16 v[2:17], v[122:125], v[118:121], v[2:17]
	ds_read_b128 v[114:117], v142
	ds_read_b128 v[118:121], v142 offset:4096
	ds_read_b128 v[122:125], v146 offset:4096
	buffer_load_dwordx4 v72, s[4:7], s31 offen lds
	s_add_i32 m0, s19, 0x2000
	s_nop 0
	buffer_load_dwordx4 v74, s[4:7], s31 offen lds
	s_add_i32 m0, s19, 0x4000
	s_waitcnt lgkmcnt(2)
	v_mfma_f32_32x32x16_f16 v[50:65], v[110:113], v[114:117], v[50:65]
	buffer_load_dwordx4 v73, s[12:15], s31 offen lds
	s_add_i32 m0, s19, 0x6000
	s_nop 0
	buffer_load_dwordx4 v75, s[12:15], s31 offen lds
	s_waitcnt vmcnt(8)
	s_barrier
	s_add_i32 s31, s0, 0x200
	s_waitcnt lgkmcnt(1)
	v_mfma_f32_32x32x16_f16 v[18:33], v[110:113], v[118:121], v[18:33]
	s_mov_b32 m0, s1
	s_abs_i32 s1, s23
	s_ashr_i32 s0, s23, 31
	s_xor_b32 s0, s0, s25
	s_waitcnt lgkmcnt(0)
	v_mfma_f32_32x32x16_f16 v[2:17], v[122:125], v[118:121], v[2:17]
	v_mfma_f32_32x32x16_f16 v[34:49], v[122:125], v[114:117], v[34:49]
	ds_read_b128 v[110:113], v67 offset:16384
	ds_read_b128 v[114:117], v109
	ds_read_b128 v[118:121], v109 offset:4096
	ds_read_b128 v[122:125], v67 offset:20480
	s_waitcnt lgkmcnt(2)
	v_mfma_f32_32x32x16_f16 v[50:65], v[110:113], v[114:117], v[50:65]
	s_waitcnt lgkmcnt(1)
	v_mfma_f32_32x32x16_f16 v[18:33], v[110:113], v[118:121], v[18:33]
	s_waitcnt lgkmcnt(0)
	v_mfma_f32_32x32x16_f16 v[2:17], v[122:125], v[118:121], v[2:17]
	v_mfma_f32_32x32x16_f16 v[34:49], v[122:125], v[114:117], v[34:49]
	ds_read_b128 v[110:113], v126 offset:16384
	ds_read_b128 v[114:117], v127
	ds_read_b128 v[118:121], v127 offset:4096
	ds_read_b128 v[122:125], v126 offset:20480
	buffer_load_dwordx4 v72, s[4:7], s31 offen lds
	s_mov_b32 m0, s2
	s_mul_hi_u32 s2, s1, s26
	buffer_load_dwordx4 v74, s[4:7], s31 offen lds
	s_mov_b32 m0, s3
	s_mul_i32 s3, s2, s24
	s_waitcnt lgkmcnt(2)
	v_mfma_f32_32x32x16_f16 v[50:65], v[110:113], v[114:117], v[50:65]
	buffer_load_dwordx4 v73, s[12:15], s31 offen lds
	s_mov_b32 m0, s18
	s_sub_i32 s1, s1, s3
	buffer_load_dwordx4 v75, s[12:15], s31 offen lds
	s_waitcnt vmcnt(8)
	s_barrier
	s_add_i32 s3, s2, 1
	s_waitcnt lgkmcnt(1)
	v_mfma_f32_32x32x16_f16 v[18:33], v[110:113], v[118:121], v[18:33]
	s_sub_i32 s14, s1, s24
	s_cmp_ge_u32 s1, s24
	s_cselect_b32 s2, s3, s2
	s_cselect_b32 s1, s14, s1
	s_add_i32 s3, s2, 1
	s_cmp_ge_u32 s1, s24
	s_cselect_b32 s1, s3, s2
	s_waitcnt lgkmcnt(0)
	v_mfma_f32_32x32x16_f16 v[2:17], v[122:125], v[118:121], v[2:17]
	s_xor_b32 s1, s1, s0
	s_sub_i32 s0, s1, s0
	s_mul_i32 s1, s0, s21
	s_sub_i32 s15, s23, s1
	s_lshl_b32 s2, s15, 7
	s_lshl_b32 s14, s0, 7
	s_ashr_i32 s3, s2, 31
	v_mfma_f32_32x32x16_f16 v[34:49], v[122:125], v[114:117], v[34:49]
	ds_read_b128 v[110:113], v67 offset:49152
	ds_read_b128 v[114:117], v109 offset:32768
	ds_read_b128 v[118:121], v109 offset:36864
	ds_read_b128 v[122:125], v67 offset:53248
	s_waitcnt lgkmcnt(2)
	v_mfma_f32_32x32x16_f16 v[50:65], v[110:113], v[114:117], v[50:65]
	s_waitcnt lgkmcnt(1)
	v_mfma_f32_32x32x16_f16 v[18:33], v[110:113], v[118:121], v[18:33]
	s_waitcnt lgkmcnt(0)
	v_mfma_f32_32x32x16_f16 v[2:17], v[122:125], v[118:121], v[2:17]
	v_mfma_f32_32x32x16_f16 v[34:49], v[122:125], v[114:117], v[34:49]
	ds_read_b128 v[110:113], v126 offset:49152
	ds_read_b128 v[114:117], v127 offset:32768
	ds_read_b128 v[118:121], v127 offset:36864
	ds_read_b128 v[122:125], v126 offset:53248
	s_waitcnt vmcnt(4)
	s_barrier
	s_waitcnt lgkmcnt(2)
	v_mfma_f32_32x32x16_f16 v[50:65], v[110:113], v[114:117], v[50:65]
	s_waitcnt lgkmcnt(1)
	v_mfma_f32_32x32x16_f16 v[18:33], v[110:113], v[118:121], v[18:33]
	s_waitcnt lgkmcnt(0)
	v_mfma_f32_32x32x16_f16 v[2:17], v[122:125], v[118:121], v[2:17]
	v_mfma_f32_32x32x16_f16 v[34:49], v[122:125], v[114:117], v[34:49]
	ds_read_b128 v[110:113], v96
	ds_read_b128 v[114:117], v128
	ds_read_b128 v[118:121], v128 offset:4096
	ds_read_b128 v[122:125], v129 offset:4096
	s_waitcnt lgkmcnt(2)
	v_mfma_f32_32x32x16_f16 v[50:65], v[110:113], v[114:117], v[50:65]
	s_waitcnt lgkmcnt(1)
	v_mfma_f32_32x32x16_f16 v[18:33], v[110:113], v[118:121], v[18:33]
	s_waitcnt lgkmcnt(0)
	v_mfma_f32_32x32x16_f16 v[2:17], v[122:125], v[118:121], v[2:17]
	v_mfma_f32_32x32x16_f16 v[34:49], v[122:125], v[114:117], v[34:49]
	ds_read_b128 v[110:113], v97
	ds_read_b128 v[114:117], v130
	ds_read_b128 v[126:129], v130 offset:4096
	ds_read_b128 v[130:133], v131 offset:4096
	s_waitcnt vmcnt(0)
	s_barrier
	s_waitcnt lgkmcnt(2)
	v_mfma_f32_32x32x16_f16 v[50:65], v[110:113], v[114:117], v[50:65]
	s_waitcnt lgkmcnt(1)
	v_mfma_f32_32x32x16_f16 v[18:33], v[110:113], v[126:129], v[18:33]
	s_waitcnt lgkmcnt(0)
	v_mfma_f32_32x32x16_f16 v[2:17], v[130:133], v[126:129], v[2:17]
	v_mfma_f32_32x32x16_f16 v[34:49], v[130:133], v[114:117], v[34:49]
	ds_read_b128 v[110:113], v98
	ds_read_b128 v[114:117], v134
	ds_read_b128 v[134:137], v134 offset:4096
	ds_read_b128 v[138:141], v138 offset:4096
	s_waitcnt lgkmcnt(2)
	v_mfma_f32_32x32x16_f16 v[50:65], v[110:113], v[114:117], v[50:65]
	s_waitcnt lgkmcnt(1)
	v_mfma_f32_32x32x16_f16 v[18:33], v[110:113], v[134:137], v[18:33]
	s_waitcnt lgkmcnt(0)
	v_mfma_f32_32x32x16_f16 v[2:17], v[138:141], v[134:137], v[2:17]
	v_mfma_f32_32x32x16_f16 v[34:49], v[138:141], v[114:117], v[34:49]
	ds_read_b128 v[110:113], v99
	ds_read_b128 v[114:117], v142
	ds_read_b128 v[142:145], v142 offset:4096
	ds_read_b128 v[146:149], v146 offset:4096
	s_waitcnt lgkmcnt(0)
	s_barrier
	s_waitcnt lgkmcnt(2)
	v_mfma_f32_32x32x16_f16 v[50:65], v[110:113], v[114:117], v[50:65]
	s_nop 11
	ds_write_b128 v100, v[50:53]
	ds_write_b128 v101, v[54:57]
	s_waitcnt lgkmcnt(3)
	v_mfma_f32_32x32x16_f16 v[18:33], v[110:113], v[142:145], v[18:33]
	s_waitcnt lgkmcnt(2)
	v_mfma_f32_32x32x16_f16 v[2:17], v[146:149], v[142:145], v[2:17]
	v_mfma_f32_32x32x16_f16 v[34:49], v[146:149], v[114:117], v[34:49]
	ds_write_b128 v102, v[58:61]
	ds_write_b128 v103, v[62:65]
	s_nop 9
	ds_write_b128 v104, v[34:37]
	ds_write_b128 v105, v[38:41]
	ds_write_b128 v106, v[42:45]
	ds_write_b128 v107, v[46:49]
	ds_write_b128 v100, v[18:21] offset:16384
	ds_write_b128 v101, v[22:25] offset:16384
	ds_write_b128 v102, v[26:29] offset:16384
	ds_write_b128 v103, v[30:33] offset:16384
	ds_write_b128 v104, v[2:5] offset:16384
	ds_write_b128 v105, v[6:9] offset:16384
	ds_write_b128 v106, v[10:13] offset:16384
	ds_write_b128 v107, v[14:17] offset:16384
	v_or_b32_e32 v25, s14, v1
	s_waitcnt lgkmcnt(0)
	s_barrier
	v_mov_b64_e32 v[10:11], v[160:161]
	v_mov_b64_e32 v[12:13], v[162:163]
	v_mov_b64_e32 v[6:7], v[176:177]
	v_mov_b64_e32 v[8:9], v[178:179]
	v_mov_b64_e32 v[2:3], v[180:181]
	v_mov_b64_e32 v[4:5], v[182:183]
	v_add_u32_e32 v14, 0, v85
	v_add_u32_e32 v18, s28, v85
	ds_read_b128 v[14:17], v14
	ds_read_b128 v[26:29], v18
	v_mov_b64_e32 v[18:19], v[164:165]
	v_mov_b64_e32 v[20:21], v[166:167]
	s_waitcnt lgkmcnt(0)
	v_pk_add_f32 v[16:17], v[16:17], v[28:29]
	v_add_f32_e32 v35, v14, v26
	v_mov_b32_e32 v34, v27
	v_cvt_f32_f16_e32 v30, v11
	v_cvt_f32_f16_sdwa v31, v11 dst_sel:DWORD dst_unused:UNUSED_PAD src0_sel:WORD_1
	v_add_u32_e32 v11, 0, v86
	v_pk_add_f32 v[16:17], v[8:9], v[16:17]
	ds_read_b128 v[26:29], v11
	v_add_u32_e32 v11, s28, v86
	v_pk_add_f32 v[36:37], v[16:17], v[30:31]
	ds_read_b128 v[30:33], v11
	v_cvt_f32_f16_e32 v38, v13
	v_cvt_f32_f16_sdwa v39, v13 dst_sel:DWORD dst_unused:UNUSED_PAD src0_sel:WORD_1
	v_mov_b32_e32 v16, v2
	v_mov_b32_e32 v17, v3
	s_waitcnt lgkmcnt(0)
	v_pk_add_f32 v[28:29], v[28:29], v[32:33]
	v_cvt_f32_f16_e32 v32, v10
	v_pk_add_f32 v[28:29], v[4:5], v[28:29]
	v_pk_mov_b32 v[16:17], v[26:27], v[16:17] op_sel:[1,0]
	v_pk_add_f32 v[28:29], v[28:29], v[38:39]
	v_cvt_f32_f16_e32 v38, v12
	v_add_f32_e32 v26, v26, v30
	v_cvt_f32_f16_sdwa v33, v10 dst_sel:DWORD dst_unused:UNUSED_PAD src0_sel:WORD_1
	v_cvt_f32_f16_sdwa v30, v12 dst_sel:DWORD dst_unused:UNUSED_PAD src0_sel:WORD_1
	v_pk_mov_b32 v[14:15], v[14:15], v[6:7] op_sel:[1,0]
	v_mov_b32_e32 v10, v31
	v_mov_b32_e32 v11, v26
	v_pk_add_f32 v[44:45], v[14:15], v[34:35]
	v_mov_b32_e32 v12, v7
	v_mov_b32_e32 v13, v32
	v_pk_add_f32 v[10:11], v[16:17], v[10:11]
	v_pk_add_f32 v[46:47], v[12:13], v[44:45]
	v_mov_b32_e32 v22, v3
	v_mov_b32_e32 v23, v38
	v_pk_add_f32 v[48:49], v[22:23], v[10:11]
	v_mov_b32_e32 v10, v33
	v_mov_b32_e32 v11, v47
	v_pk_add_f32 v[50:51], v[46:47], v[10:11]
	v_mov_b64_e32 v[14:15], v[168:169]
	v_mov_b64_e32 v[16:17], v[170:171]
	v_mov_b64_e32 v[10:11], v[172:173]
	v_mov_b64_e32 v[12:13], v[174:175]
	v_mov_b32_e32 v31, v49
	v_pk_add_f32 v[40:41], v[48:49], v[30:31]
	v_pk_mov_b32 v[30:31], v[34:35], v[44:45] op_sel:[1,0]
	v_mov_b32_e32 v27, v44
	v_mov_b32_e32 v3, v7
	v_pk_add_f32 v[30:31], v[6:7], v[30:31]
	v_mov_b32_e32 v39, v33
	v_pk_add_f32 v[26:27], v[2:3], v[26:27]
	v_pk_add_f32 v[30:31], v[30:31], v[32:33]
	v_pk_add_f32 v[26:27], v[26:27], v[38:39]
	v_pk_mul_f32 v[32:33], v[46:47], v[46:47]
	v_pk_add_f32 v[34:35], v[30:31], v[26:27]
	v_pk_mul_f32 v[26:27], v[30:31], v[26:27]
	v_mov_b32_e32 v51, v33
	v_pk_mul_f32 v[32:33], v[48:49], v[48:49]
	v_mov_b32_e32 v35, v27
	v_pk_mul_f32 v[26:27], v[40:41], v[40:41]
	v_mov_b32_e32 v32, v40
	v_mov_b32_e32 v67, v26
	v_pk_add_f32 v[32:33], v[50:51], v[32:33]
	v_pk_add_f32 v[26:27], v[34:35], v[66:67]
	v_pk_mul_f32 v[30:31], v[36:37], v[36:37]
	v_pk_mul_f32 v[34:35], v[28:29], v[28:29]
	v_pk_add_f32 v[26:27], v[32:33], v[26:27]
	v_mov_b32_e32 v32, v36
	v_mov_b32_e32 v33, v30
	v_mov_b32_e32 v38, v28
	v_mov_b32_e32 v39, v34
	v_pk_add_f32 v[32:33], v[32:33], v[38:39]
	v_mov_b32_e32 v30, v37
	v_mov_b32_e32 v34, v29
	v_pk_add_f32 v[26:27], v[26:27], v[32:33]
	v_pk_add_f32 v[30:31], v[30:31], v[34:35]
	v_pk_add_f32 v[26:27], v[26:27], v[30:31]
	s_nop 1
	v_mov_b32_dpp v32, v26 row_mirror row_mask:0xf bank_mask:0xf
	v_mov_b32_dpp v33, v27 row_mirror row_mask:0xf bank_mask:0xf
	v_cvt_pk_f16_f32 v39, v28, v29
	v_or_b32_e32 v31, s2, v78
	s_waitcnt lgkmcnt(0)
	v_pk_add_f32 v[26:27], v[26:27], v[32:33]
	s_nop 1
	v_mov_b32_dpp v34, v26 row_half_mirror row_mask:0xf bank_mask:0xf
	v_mov_b32_dpp v35, v27 row_half_mirror row_mask:0xf bank_mask:0xf
	v_cvt_pk_f16_f32 v37, v36, v37
	v_cvt_pk_f16_f32 v36, v47, v50
	s_waitcnt lgkmcnt(0)
	v_pk_add_f32 v[26:27], v[26:27], v[34:35]
	s_nop 1
	v_mov_b32_dpp v28, v26 quad_perm:[2,3,0,1] row_mask:0xf bank_mask:0xf
	v_mov_b32_dpp v29, v27 quad_perm:[2,3,0,1] row_mask:0xf bank_mask:0xf
	v_mul_lo_u32 v24, v25, s30
	v_add_lshl_u32 v24, v31, v24, 1
	v_cvt_pk_f16_f32 v38, v49, v40
	buffer_store_dwordx4 v[36:39], v24, s[8:11], 0 offen sc1
	s_waitcnt lgkmcnt(0)
	v_pk_add_f32 v[26:27], v[26:27], v[28:29]
	s_lshl_b32 s2, s15, 4
	v_mov_b32_e32 v24, v7
	s_nop 1
	v_mov_b32_dpp v28, v26 quad_perm:[1,0,3,2] row_mask:0xf bank_mask:0xf
	v_mov_b32_dpp v29, v27 quad_perm:[1,0,3,2] row_mask:0xf bank_mask:0xf
	s_and_saveexec_b64 s[0:1], vcc
	s_cbranch_execz .LBB7_5
	s_waitcnt lgkmcnt(0)
	v_pk_add_f32 v[64:65], v[26:27], v[28:29]
	v_lshl_add_u32 v23, v25, 6, s2
	v_mov_b32_e32 v67, v66
	s_mov_b32 s18, s10
	s_mov_b32 s19, s11
	buffer_store_dwordx4 v[64:67], v23, s[16:19], 0 offen sc1

.LBB9_3:
	s_ff1_i32_b32 s44, s21
	s_lshr_b32 s45, s23, s44
	s_lshl_b32 s46, s45, 7
	s_mul_i32 s47, s45, s21
	s_sub_i32 s47, s23, s47
	s_lshl_b32 s48, s47, 7
	s_ashr_i32 s49, s48, 31
	v_or_b32_e32 v152, s46, v1
	v_lshl_add_u64 v[154:155], s[48:49], 1, v[70:71]
	v_mad_i64_i32 v[156:157], s[50:51], v152, s29, v[154:155]
	v_lshl_add_u64 v[158:159], s[48:49], 2, v[68:69]
	v_or_b32_e32 v153, 32, v152
	global_load_dwordx4 v[160:163], v[156:157], off
	v_mad_i64_i32 v[184:185], s[50:51], v153, s29, v[154:155]
	v_or_b32_e32 v153, 64, v152
	global_load_dwordx4 v[176:179], v[158:159], off
	global_load_dwordx4 v[180:183], v[158:159], off offset:16
	v_mad_i64_i32 v[186:187], s[50:51], v153, s29, v[154:155]
	v_or_b32_e32 v153, 0x60, v152
	global_load_dwordx4 v[164:167], v[184:185], off
	v_mad_i64_i32 v[188:189], s[50:51], v153, s29, v[154:155]
	global_load_dwordx4 v[168:171], v[186:187], off
	s_nop 0
	global_load_dwordx4 v[172:175], v[188:189], off
	v_add_u32_e32 v110, v80, v76
	s_waitcnt vmcnt(14)
	s_barrier
	s_waitcnt lgkmcnt(0)
	ds_read_b128 v[2:5], v110 offset:16384
	v_add_u32_e32 v111, v79, v76
	ds_read_b128 v[6:9], v111
	ds_read_b128 v[10:13], v111 offset:4096
	ds_read_b128 v[14:17], v110 offset:20480
	v_add_u32_e32 v67, v80, v77
	ds_read_b128 v[34:37], v67 offset:16384
	v_add_u32_e32 v109, v79, v77
	s_waitcnt lgkmcnt(3)
	v_mfma_f32_32x32x16_f16 v[50:65], v[2:5], v[6:9], 0
	ds_read_b128 v[112:115], v109
	ds_read_b128 v[116:119], v109 offset:4096
	ds_read_b128 v[120:123], v67 offset:20480
	v_readfirstlane_b32 s2, v0
	s_lshl_b32 s35, s27, 15
	s_lshl_b32 s2, s2, 4
	s_add_i32 s1, s35, 0
	s_and_b32 s39, s2, 0xfffffc00
	s_add_i32 s1, s1, s39
	s_waitcnt lgkmcnt(5)
	v_mfma_f32_32x32x16_f16 v[18:33], v[2:5], v[10:13], 0
	s_mov_b32 m0, s1
	s_add_i32 s2, s1, 0x2000
	buffer_load_dwordx4 v72, s[4:7], s0 offen lds
	s_mov_b32 m0, s2
	s_add_i32 s3, s1, 0x4000
	buffer_load_dwordx4 v74, s[4:7], s0 offen lds
	s_mov_b32 s14, s10
	s_waitcnt lgkmcnt(2)
	v_mfma_f32_32x32x16_f16 v[50:65], v[34:37], v[112:115], v[50:65]
	s_mov_b32 s15, s11
	s_mov_b32 m0, s3
	s_add_i32 s18, s1, 0x6000
	buffer_load_dwordx4 v73, s[12:15], s0 offen lds
	s_mov_b32 m0, s18
	s_add_i32 s19, s35, 0x8000
	buffer_load_dwordx4 v75, s[12:15], s0 offen lds
	s_waitcnt lgkmcnt(1)
	v_mfma_f32_32x32x16_f16 v[18:33], v[34:37], v[116:119], v[18:33]
	s_waitcnt vmcnt(14)
	s_barrier
	s_and_b32 s19, s19, 0x18000
	s_add_i32 s19, s19, 0
	s_add_i32 s19, s19, s39
	s_add_i32 s36, s0, 0x80
	s_mov_b32 m0, s19
	v_mfma_f32_32x32x16_f16 v[34:49], v[14:17], v[6:9], 0
	s_add_i32 s31, s19, 0x2000
	s_add_i32 s33, s19, 0x4000
	s_add_i32 s34, s19, 0x6000
	s_xor_b32 s40, s35, 0x10000
	s_add_i32 s35, s40, 0
	s_add_i32 s35, s35, s39
	s_add_i32 s41, s0, 0x100
	v_mfma_f32_32x32x16_f16 v[2:17], v[14:17], v[10:13], 0
	s_add_i32 s37, s35, 0x4000
	s_add_i32 s38, s35, 0x6000
	s_add_i32 s40, s40, 0x8000
	s_and_b32 s40, s40, 0x18000
	s_add_i32 s40, s40, 0
	s_add_i32 s39, s40, s39
	s_add_i32 s43, s0, 0x180
	s_waitcnt lgkmcnt(0)
	v_mfma_f32_32x32x16_f16 v[34:49], v[120:123], v[112:115], v[34:49]
	s_add_i32 s40, s39, 0x2000
	s_add_i32 s42, s39, 0x6000
	v_mfma_f32_32x32x16_f16 v[2:17], v[120:123], v[116:119], v[2:17]
	ds_read_b128 v[112:115], v110 offset:49152
	ds_read_b128 v[116:119], v111 offset:32768
	ds_read_b128 v[120:123], v111 offset:36864
	ds_read_b128 v[124:127], v110 offset:53248
	s_waitcnt lgkmcnt(2)
	v_mfma_f32_32x32x16_f16 v[50:65], v[112:115], v[116:119], v[50:65]
	s_waitcnt lgkmcnt(1)
	v_mfma_f32_32x32x16_f16 v[18:33], v[112:115], v[120:123], v[18:33]
	s_waitcnt lgkmcnt(0)
	v_mfma_f32_32x32x16_f16 v[34:49], v[124:127], v[116:119], v[34:49]
	v_mfma_f32_32x32x16_f16 v[2:17], v[124:127], v[120:123], v[2:17]
	ds_read_b128 v[112:115], v67 offset:49152
	ds_read_b128 v[116:119], v109 offset:32768
	ds_read_b128 v[120:123], v109 offset:36864
	ds_read_b128 v[124:127], v67 offset:53248
	buffer_load_dwordx4 v72, s[4:7], s36 offen lds
	s_mov_b32 m0, s31
	s_nop 0
	buffer_load_dwordx4 v74, s[4:7], s36 offen lds
	s_mov_b32 m0, s33
	s_nop 0
	buffer_load_dwordx4 v73, s[12:15], s36 offen lds
	s_mov_b32 m0, s34
	s_waitcnt lgkmcnt(2)
	v_mfma_f32_32x32x16_f16 v[50:65], v[112:115], v[116:119], v[50:65]
	buffer_load_dwordx4 v75, s[12:15], s36 offen lds
	s_waitcnt vmcnt(14)
	s_barrier
	s_mov_b32 m0, s35
	s_add_i32 s36, s35, 0x2000
	s_waitcnt lgkmcnt(1)
	v_mfma_f32_32x32x16_f16 v[18:33], v[112:115], v[120:123], v[18:33]
	v_add_u32_e32 v113, v81, v76
	v_add_u32_e32 v112, v82, v76
	s_waitcnt lgkmcnt(0)
	v_mfma_f32_32x32x16_f16 v[34:49], v[124:127], v[116:119], v[34:49]
	ds_read_b128 v[114:117], v96
	v_mfma_f32_32x32x16_f16 v[2:17], v[124:127], v[120:123], v[2:17]
	ds_read_b128 v[118:121], v113
	ds_read_b128 v[122:125], v113 offset:4096
	ds_read_b128 v[126:129], v112 offset:4096
	s_waitcnt lgkmcnt(2)
	v_mfma_f32_32x32x16_f16 v[50:65], v[114:117], v[118:121], v[50:65]
	s_waitcnt lgkmcnt(1)
	v_mfma_f32_32x32x16_f16 v[18:33], v[114:117], v[122:125], v[18:33]
	v_add_u32_e32 v115, v81, v77
	v_add_u32_e32 v114, v82, v77
	s_waitcnt lgkmcnt(0)
	v_mfma_f32_32x32x16_f16 v[34:49], v[126:129], v[118:121], v[34:49]
	ds_read_b128 v[116:119], v97
	v_mfma_f32_32x32x16_f16 v[2:17], v[126:129], v[122:125], v[2:17]
	ds_read_b128 v[120:123], v115
	ds_read_b128 v[124:127], v115 offset:4096
	ds_read_b128 v[128:131], v114 offset:4096
	buffer_load_dwordx4 v72, s[4:7], s41 offen lds
	s_mov_b32 m0, s36
	s_nop 0
	buffer_load_dwordx4 v74, s[4:7], s41 offen lds
	s_mov_b32 m0, s37
	s_waitcnt lgkmcnt(2)
	v_mfma_f32_32x32x16_f16 v[50:65], v[116:119], v[120:123], v[50:65]
	buffer_load_dwordx4 v73, s[12:15], s41 offen lds
	s_mov_b32 m0, s38
	s_nop 0
	buffer_load_dwordx4 v75, s[12:15], s41 offen lds
	s_waitcnt vmcnt(8)
	s_barrier
	s_mov_b32 m0, s39
	s_waitcnt lgkmcnt(1)
	v_mfma_f32_32x32x16_f16 v[18:33], v[116:119], v[124:127], v[18:33]
	v_add_u32_e32 v117, v83, v76
	v_add_u32_e32 v116, v84, v76
	s_add_i32 s41, s39, 0x4000
	s_waitcnt lgkmcnt(0)
	v_mfma_f32_32x32x16_f16 v[34:49], v[128:131], v[120:123], v[34:49]
	ds_read_b128 v[118:121], v98
	v_mfma_f32_32x32x16_f16 v[2:17], v[128:131], v[124:127], v[2:17]
	ds_read_b128 v[122:125], v117
	ds_read_b128 v[126:129], v117 offset:4096
	ds_read_b128 v[130:133], v116 offset:4096
	s_waitcnt lgkmcnt(2)
	v_mfma_f32_32x32x16_f16 v[50:65], v[118:121], v[122:125], v[50:65]
	s_waitcnt lgkmcnt(1)
	v_mfma_f32_32x32x16_f16 v[18:33], v[118:121], v[126:129], v[18:33]
	v_add_u32_e32 v119, v83, v77
	v_add_u32_e32 v118, v84, v77
	s_waitcnt lgkmcnt(0)
	v_mfma_f32_32x32x16_f16 v[34:49], v[130:133], v[122:125], v[34:49]
	ds_read_b128 v[120:123], v99
	v_mfma_f32_32x32x16_f16 v[2:17], v[130:133], v[126:129], v[2:17]
	ds_read_b128 v[124:127], v119
	ds_read_b128 v[128:131], v119 offset:4096
	ds_read_b128 v[132:135], v118 offset:4096
	buffer_load_dwordx4 v72, s[4:7], s43 offen lds
	s_mov_b32 m0, s40
	s_nop 0
	buffer_load_dwordx4 v74, s[4:7], s43 offen lds
	s_mov_b32 m0, s41
	s_waitcnt lgkmcnt(2)
	v_mfma_f32_32x32x16_f16 v[50:65], v[120:123], v[124:127], v[50:65]
	buffer_load_dwordx4 v73, s[12:15], s43 offen lds
	s_mov_b32 m0, s42
	s_nop 0
	buffer_load_dwordx4 v75, s[12:15], s43 offen lds
	s_waitcnt vmcnt(8)
	s_barrier
	s_add_i32 s43, s0, 0x200
	s_waitcnt lgkmcnt(1)
	v_mfma_f32_32x32x16_f16 v[18:33], v[120:123], v[128:131], v[18:33]
	s_mov_b32 m0, s1
	s_waitcnt lgkmcnt(0)
	v_mfma_f32_32x32x16_f16 v[34:49], v[132:135], v[124:127], v[34:49]
	v_mfma_f32_32x32x16_f16 v[2:17], v[132:135], v[128:131], v[2:17]
	ds_read_b128 v[120:123], v110 offset:16384
	ds_read_b128 v[124:127], v111
	ds_read_b128 v[128:131], v111 offset:4096
	ds_read_b128 v[132:135], v110 offset:20480
	s_waitcnt lgkmcnt(2)
	v_mfma_f32_32x32x16_f16 v[50:65], v[120:123], v[124:127], v[50:65]
	s_waitcnt lgkmcnt(1)
	v_mfma_f32_32x32x16_f16 v[18:33], v[120:123], v[128:131], v[18:33]
	s_waitcnt lgkmcnt(0)
	v_mfma_f32_32x32x16_f16 v[34:49], v[132:135], v[124:127], v[34:49]
	v_mfma_f32_32x32x16_f16 v[2:17], v[132:135], v[128:131], v[2:17]
	ds_read_b128 v[120:123], v67 offset:16384
	ds_read_b128 v[124:127], v109
	ds_read_b128 v[128:131], v109 offset:4096
	ds_read_b128 v[132:135], v67 offset:20480
	buffer_load_dwordx4 v72, s[4:7], s43 offen lds
	s_mov_b32 m0, s2
	s_nop 0
	buffer_load_dwordx4 v74, s[4:7], s43 offen lds
	s_mov_b32 m0, s3
	s_waitcnt lgkmcnt(2)
	v_mfma_f32_32x32x16_f16 v[50:65], v[120:123], v[124:127], v[50:65]
	buffer_load_dwordx4 v73, s[12:15], s43 offen lds
	s_mov_b32 m0, s18
	s_nop 0
	buffer_load_dwordx4 v75, s[12:15], s43 offen lds
	s_waitcnt vmcnt(8)
	s_barrier
	s_add_i32 s43, s0, 0x280
	s_waitcnt lgkmcnt(1)
	v_mfma_f32_32x32x16_f16 v[18:33], v[120:123], v[128:131], v[18:33]
	s_mov_b32 m0, s19
	s_waitcnt lgkmcnt(0)
	v_mfma_f32_32x32x16_f16 v[34:49], v[132:135], v[124:127], v[34:49]
	v_mfma_f32_32x32x16_f16 v[2:17], v[132:135], v[128:131], v[2:17]
	ds_read_b128 v[120:123], v110 offset:49152
	ds_read_b128 v[124:127], v111 offset:32768
	ds_read_b128 v[128:131], v111 offset:36864
	ds_read_b128 v[132:135], v110 offset:53248
	s_waitcnt lgkmcnt(2)
	v_mfma_f32_32x32x16_f16 v[50:65], v[120:123], v[124:127], v[50:65]
	s_waitcnt lgkmcnt(1)
	v_mfma_f32_32x32x16_f16 v[18:33], v[120:123], v[128:131], v[18:33]
	s_waitcnt lgkmcnt(0)
	v_mfma_f32_32x32x16_f16 v[34:49], v[132:135], v[124:127], v[34:49]
	v_mfma_f32_32x32x16_f16 v[2:17], v[132:135], v[128:131], v[2:17]
	ds_read_b128 v[120:123], v67 offset:49152
	ds_read_b128 v[124:127], v109 offset:32768
	ds_read_b128 v[128:131], v109 offset:36864
	ds_read_b128 v[132:135], v67 offset:53248
	buffer_load_dwordx4 v72, s[4:7], s43 offen lds
	s_mov_b32 m0, s31
	s_nop 0
	buffer_load_dwordx4 v74, s[4:7], s43 offen lds
	s_mov_b32 m0, s33
	s_waitcnt lgkmcnt(2)
	v_mfma_f32_32x32x16_f16 v[50:65], v[120:123], v[124:127], v[50:65]
	buffer_load_dwordx4 v73, s[12:15], s43 offen lds
	s_mov_b32 m0, s34
	s_nop 0
	buffer_load_dwordx4 v75, s[12:15], s43 offen lds
	s_waitcnt vmcnt(8)
	s_barrier
	s_add_i32 s43, s0, 0x300
	s_waitcnt lgkmcnt(1)
	v_mfma_f32_32x32x16_f16 v[18:33], v[120:123], v[128:131], v[18:33]
	s_mov_b32 m0, s35
	s_waitcnt lgkmcnt(0)
	v_mfma_f32_32x32x16_f16 v[34:49], v[132:135], v[124:127], v[34:49]
	v_mfma_f32_32x32x16_f16 v[2:17], v[132:135], v[128:131], v[2:17]
	ds_read_b128 v[120:123], v96
	ds_read_b128 v[124:127], v113
	ds_read_b128 v[128:131], v113 offset:4096
	ds_read_b128 v[132:135], v112 offset:4096
	s_waitcnt lgkmcnt(2)
	v_mfma_f32_32x32x16_f16 v[50:65], v[120:123], v[124:127], v[50:65]
	s_waitcnt lgkmcnt(1)
	v_mfma_f32_32x32x16_f16 v[18:33], v[120:123], v[128:131], v[18:33]
	s_waitcnt lgkmcnt(0)
	v_mfma_f32_32x32x16_f16 v[34:49], v[132:135], v[124:127], v[34:49]
	v_mfma_f32_32x32x16_f16 v[2:17], v[132:135], v[128:131], v[2:17]
	ds_read_b128 v[120:123], v97
	ds_read_b128 v[124:127], v115
	ds_read_b128 v[128:131], v115 offset:4096
	ds_read_b128 v[132:135], v114 offset:4096
	buffer_load_dwordx4 v72, s[4:7], s43 offen lds
	s_mov_b32 m0, s36
	s_nop 0
	buffer_load_dwordx4 v74, s[4:7], s43 offen lds
	s_mov_b32 m0, s37
	s_waitcnt lgkmcnt(2)
	v_mfma_f32_32x32x16_f16 v[50:65], v[120:123], v[124:127], v[50:65]
	buffer_load_dwordx4 v73, s[12:15], s43 offen lds
	s_mov_b32 m0, s38
	s_nop 0
	buffer_load_dwordx4 v75, s[12:15], s43 offen lds
	s_waitcnt vmcnt(8)
	s_barrier
	s_add_i32 s43, s0, 0x380
	s_waitcnt lgkmcnt(1)
	v_mfma_f32_32x32x16_f16 v[18:33], v[120:123], v[128:131], v[18:33]
	s_mov_b32 m0, s39
	s_waitcnt lgkmcnt(0)
	v_mfma_f32_32x32x16_f16 v[34:49], v[132:135], v[124:127], v[34:49]
	v_mfma_f32_32x32x16_f16 v[2:17], v[132:135], v[128:131], v[2:17]
	ds_read_b128 v[120:123], v98
	ds_read_b128 v[124:127], v117
	ds_read_b128 v[128:131], v117 offset:4096
	ds_read_b128 v[132:135], v116 offset:4096
	s_waitcnt lgkmcnt(2)
	v_mfma_f32_32x32x16_f16 v[50:65], v[120:123], v[124:127], v[50:65]
	s_waitcnt lgkmcnt(1)
	v_mfma_f32_32x32x16_f16 v[18:33], v[120:123], v[128:131], v[18:33]
	s_waitcnt lgkmcnt(0)
	v_mfma_f32_32x32x16_f16 v[34:49], v[132:135], v[124:127], v[34:49]
	v_mfma_f32_32x32x16_f16 v[2:17], v[132:135], v[128:131], v[2:17]
	ds_read_b128 v[120:123], v99
	ds_read_b128 v[124:127], v119
	ds_read_b128 v[128:131], v119 offset:4096
	ds_read_b128 v[132:135], v118 offset:4096
	buffer_load_dwordx4 v72, s[4:7], s43 offen lds
	s_mov_b32 m0, s40
	s_nop 0
	buffer_load_dwordx4 v74, s[4:7], s43 offen lds
	s_mov_b32 m0, s41
	s_waitcnt lgkmcnt(2)
	v_mfma_f32_32x32x16_f16 v[50:65], v[120:123], v[124:127], v[50:65]
	buffer_load_dwordx4 v73, s[12:15], s43 offen lds
	s_mov_b32 m0, s42
	s_nop 0
	buffer_load_dwordx4 v75, s[12:15], s43 offen lds
	s_waitcnt vmcnt(8)
	s_barrier
	s_add_i32 s43, s0, 0x400
	s_waitcnt lgkmcnt(1)
	v_mfma_f32_32x32x16_f16 v[18:33], v[120:123], v[128:131], v[18:33]
	s_mov_b32 m0, s1
	s_waitcnt lgkmcnt(0)
	v_mfma_f32_32x32x16_f16 v[34:49], v[132:135], v[124:127], v[34:49]
	v_mfma_f32_32x32x16_f16 v[2:17], v[132:135], v[128:131], v[2:17]
	ds_read_b128 v[120:123], v110 offset:16384
	ds_read_b128 v[124:127], v111
	ds_read_b128 v[128:131], v111 offset:4096
	ds_read_b128 v[132:135], v110 offset:20480
	s_waitcnt lgkmcnt(2)
	v_mfma_f32_32x32x16_f16 v[50:65], v[120:123], v[124:127], v[50:65]
	s_waitcnt lgkmcnt(1)
	v_mfma_f32_32x32x16_f16 v[18:33], v[120:123], v[128:131], v[18:33]
	s_waitcnt lgkmcnt(0)
	v_mfma_f32_32x32x16_f16 v[34:49], v[132:135], v[124:127], v[34:49]
	v_mfma_f32_32x32x16_f16 v[2:17], v[132:135], v[128:131], v[2:17]
	ds_read_b128 v[120:123], v67 offset:16384
	ds_read_b128 v[124:127], v109
	ds_read_b128 v[128:131], v109 offset:4096
	ds_read_b128 v[132:135], v67 offset:20480
	buffer_load_dwordx4 v72, s[4:7], s43 offen lds
	s_mov_b32 m0, s2
	s_nop 0
	buffer_load_dwordx4 v74, s[4:7], s43 offen lds
	s_mov_b32 m0, s3
	s_waitcnt lgkmcnt(2)
	v_mfma_f32_32x32x16_f16 v[50:65], v[120:123], v[124:127], v[50:65]
	buffer_load_dwordx4 v73, s[12:15], s43 offen lds
	s_mov_b32 m0, s18
	s_nop 0
	buffer_load_dwordx4 v75, s[12:15], s43 offen lds
	s_waitcnt vmcnt(8)
	s_barrier
	s_add_i32 s43, s0, 0x480
	s_waitcnt lgkmcnt(1)
	v_mfma_f32_32x32x16_f16 v[18:33], v[120:123], v[128:131], v[18:33]
	s_mov_b32 m0, s19
	s_waitcnt lgkmcnt(0)
	v_mfma_f32_32x32x16_f16 v[34:49], v[132:135], v[124:127], v[34:49]
	v_mfma_f32_32x32x16_f16 v[2:17], v[132:135], v[128:131], v[2:17]
	ds_read_b128 v[120:123], v110 offset:49152
	ds_read_b128 v[124:127], v111 offset:32768
	ds_read_b128 v[128:131], v111 offset:36864
	ds_read_b128 v[132:135], v110 offset:53248
	s_waitcnt lgkmcnt(2)
	v_mfma_f32_32x32x16_f16 v[50:65], v[120:123], v[124:127], v[50:65]
	s_waitcnt lgkmcnt(1)
	v_mfma_f32_32x32x16_f16 v[18:33], v[120:123], v[128:131], v[18:33]
	s_waitcnt lgkmcnt(0)
	v_mfma_f32_32x32x16_f16 v[34:49], v[132:135], v[124:127], v[34:49]
	v_mfma_f32_32x32x16_f16 v[2:17], v[132:135], v[128:131], v[2:17]
	ds_read_b128 v[120:123], v67 offset:49152
	ds_read_b128 v[124:127], v109 offset:32768
	ds_read_b128 v[128:131], v109 offset:36864
	ds_read_b128 v[132:135], v67 offset:53248
	buffer_load_dwordx4 v72, s[4:7], s43 offen lds
	s_mov_b32 m0, s31
	s_nop 0
	buffer_load_dwordx4 v74, s[4:7], s43 offen lds
	s_mov_b32 m0, s33
	s_waitcnt lgkmcnt(2)
	v_mfma_f32_32x32x16_f16 v[50:65], v[120:123], v[124:127], v[50:65]
	buffer_load_dwordx4 v73, s[12:15], s43 offen lds
	s_mov_b32 m0, s34
	s_nop 0
	buffer_load_dwordx4 v75, s[12:15], s43 offen lds
	s_waitcnt vmcnt(8)
	s_barrier
	s_add_i32 s43, s0, 0x500
	s_waitcnt lgkmcnt(1)
	v_mfma_f32_32x32x16_f16 v[18:33], v[120:123], v[128:131], v[18:33]
	s_mov_b32 m0, s35
	s_waitcnt lgkmcnt(0)
	v_mfma_f32_32x32x16_f16 v[34:49], v[132:135], v[124:127], v[34:49]
	v_mfma_f32_32x32x16_f16 v[2:17], v[132:135], v[128:131], v[2:17]
	ds_read_b128 v[120:123], v96
	ds_read_b128 v[124:127], v113
	ds_read_b128 v[128:131], v113 offset:4096
	ds_read_b128 v[132:135], v112 offset:4096
	s_waitcnt lgkmcnt(2)
	v_mfma_f32_32x32x16_f16 v[50:65], v[120:123], v[124:127], v[50:65]
	s_waitcnt lgkmcnt(1)
	v_mfma_f32_32x32x16_f16 v[18:33], v[120:123], v[128:131], v[18:33]
	s_waitcnt lgkmcnt(0)
	v_mfma_f32_32x32x16_f16 v[34:49], v[132:135], v[124:127], v[34:49]
	v_mfma_f32_32x32x16_f16 v[2:17], v[132:135], v[128:131], v[2:17]
	ds_read_b128 v[120:123], v97
	ds_read_b128 v[124:127], v115
	ds_read_b128 v[128:131], v115 offset:4096
	ds_read_b128 v[132:135], v114 offset:4096
	buffer_load_dwordx4 v72, s[4:7], s43 offen lds
	s_mov_b32 m0, s36
	s_nop 0
	buffer_load_dwordx4 v74, s[4:7], s43 offen lds
	s_mov_b32 m0, s37
	s_waitcnt lgkmcnt(2)
	v_mfma_f32_32x32x16_f16 v[50:65], v[120:123], v[124:127], v[50:65]
	buffer_load_dwordx4 v73, s[12:15], s43 offen lds
	s_mov_b32 m0, s38
	s_nop 0
	buffer_load_dwordx4 v75, s[12:15], s43 offen lds
	s_waitcnt vmcnt(8)
	s_barrier
	s_add_i32 s43, s0, 0x580
	s_waitcnt lgkmcnt(1)
	v_mfma_f32_32x32x16_f16 v[18:33], v[120:123], v[128:131], v[18:33]
	s_mov_b32 m0, s39
	s_waitcnt lgkmcnt(0)
	v_mfma_f32_32x32x16_f16 v[34:49], v[132:135], v[124:127], v[34:49]
	v_mfma_f32_32x32x16_f16 v[2:17], v[132:135], v[128:131], v[2:17]
	ds_read_b128 v[120:123], v98
	ds_read_b128 v[124:127], v117
	ds_read_b128 v[128:131], v117 offset:4096
	ds_read_b128 v[132:135], v116 offset:4096
	s_waitcnt lgkmcnt(2)
	v_mfma_f32_32x32x16_f16 v[50:65], v[120:123], v[124:127], v[50:65]
	s_waitcnt lgkmcnt(1)
	v_mfma_f32_32x32x16_f16 v[18:33], v[120:123], v[128:131], v[18:33]
	s_waitcnt lgkmcnt(0)
	v_mfma_f32_32x32x16_f16 v[34:49], v[132:135], v[124:127], v[34:49]
	v_mfma_f32_32x32x16_f16 v[2:17], v[132:135], v[128:131], v[2:17]
	ds_read_b128 v[120:123], v99
	ds_read_b128 v[124:127], v119
	ds_read_b128 v[128:131], v119 offset:4096
	ds_read_b128 v[132:135], v118 offset:4096
	buffer_load_dwordx4 v72, s[4:7], s43 offen lds
	s_mov_b32 m0, s40
	s_nop 0
	buffer_load_dwordx4 v74, s[4:7], s43 offen lds
	s_mov_b32 m0, s41
	s_waitcnt lgkmcnt(2)
	v_mfma_f32_32x32x16_f16 v[50:65], v[120:123], v[124:127], v[50:65]
	buffer_load_dwordx4 v73, s[12:15], s43 offen lds
	s_mov_b32 m0, s42
	s_nop 0
	buffer_load_dwordx4 v75, s[12:15], s43 offen lds
	s_waitcnt vmcnt(8)
	s_barrier
	s_add_i32 s43, s0, 0x600
	s_waitcnt lgkmcnt(1)
	v_mfma_f32_32x32x16_f16 v[18:33], v[120:123], v[128:131], v[18:33]
	s_mov_b32 m0, s1
	s_waitcnt lgkmcnt(0)
	v_mfma_f32_32x32x16_f16 v[34:49], v[132:135], v[124:127], v[34:49]
	v_mfma_f32_32x32x16_f16 v[2:17], v[132:135], v[128:131], v[2:17]
	ds_read_b128 v[120:123], v110 offset:16384
	ds_read_b128 v[124:127], v111
	ds_read_b128 v[128:131], v111 offset:4096
	ds_read_b128 v[132:135], v110 offset:20480
	s_waitcnt lgkmcnt(2)
	v_mfma_f32_32x32x16_f16 v[50:65], v[120:123], v[124:127], v[50:65]
	s_waitcnt lgkmcnt(1)
	v_mfma_f32_32x32x16_f16 v[18:33], v[120:123], v[128:131], v[18:33]
	s_waitcnt lgkmcnt(0)
	v_mfma_f32_32x32x16_f16 v[34:49], v[132:135], v[124:127], v[34:49]
	v_mfma_f32_32x32x16_f16 v[2:17], v[132:135], v[128:131], v[2:17]
	ds_read_b128 v[120:123], v67 offset:16384
	ds_read_b128 v[124:127], v109
	ds_read_b128 v[128:131], v109 offset:4096
	ds_read_b128 v[132:135], v67 offset:20480
	buffer_load_dwordx4 v72, s[4:7], s43 offen lds
	s_mov_b32 m0, s2
	s_nop 0
	buffer_load_dwordx4 v74, s[4:7], s43 offen lds
	s_mov_b32 m0, s3
	s_waitcnt lgkmcnt(2)
	v_mfma_f32_32x32x16_f16 v[50:65], v[120:123], v[124:127], v[50:65]
	buffer_load_dwordx4 v73, s[12:15], s43 offen lds
	s_mov_b32 m0, s18
	s_nop 0
	buffer_load_dwordx4 v75, s[12:15], s43 offen lds
	s_waitcnt vmcnt(8)
	s_barrier
	s_add_i32 s43, s0, 0x680
	s_waitcnt lgkmcnt(1)
	v_mfma_f32_32x32x16_f16 v[18:33], v[120:123], v[128:131], v[18:33]
	s_mov_b32 m0, s19
	s_waitcnt lgkmcnt(0)
	v_mfma_f32_32x32x16_f16 v[34:49], v[132:135], v[124:127], v[34:49]
	v_mfma_f32_32x32x16_f16 v[2:17], v[132:135], v[128:131], v[2:17]
	ds_read_b128 v[120:123], v110 offset:49152
	ds_read_b128 v[124:127], v111 offset:32768
	ds_read_b128 v[128:131], v111 offset:36864
	ds_read_b128 v[132:135], v110 offset:53248
	s_waitcnt lgkmcnt(2)
	v_mfma_f32_32x32x16_f16 v[50:65], v[120:123], v[124:127], v[50:65]
	s_waitcnt lgkmcnt(1)
	v_mfma_f32_32x32x16_f16 v[18:33], v[120:123], v[128:131], v[18:33]
	s_waitcnt lgkmcnt(0)
	v_mfma_f32_32x32x16_f16 v[34:49], v[132:135], v[124:127], v[34:49]
	v_mfma_f32_32x32x16_f16 v[2:17], v[132:135], v[128:131], v[2:17]
	ds_read_b128 v[120:123], v67 offset:49152
	ds_read_b128 v[124:127], v109 offset:32768
	ds_read_b128 v[128:131], v109 offset:36864
	ds_read_b128 v[132:135], v67 offset:53248
	buffer_load_dwordx4 v72, s[4:7], s43 offen lds
	s_mov_b32 m0, s31
	s_nop 0
	buffer_load_dwordx4 v74, s[4:7], s43 offen lds
	s_mov_b32 m0, s33
	s_waitcnt lgkmcnt(2)
	v_mfma_f32_32x32x16_f16 v[50:65], v[120:123], v[124:127], v[50:65]
	buffer_load_dwordx4 v73, s[12:15], s43 offen lds
	s_mov_b32 m0, s34
	s_nop 0
	buffer_load_dwordx4 v75, s[12:15], s43 offen lds
	s_waitcnt vmcnt(8)
	s_barrier
	s_add_i32 s43, s0, 0x700
	s_waitcnt lgkmcnt(1)
	v_mfma_f32_32x32x16_f16 v[18:33], v[120:123], v[128:131], v[18:33]
	s_mov_b32 m0, s35
	s_waitcnt lgkmcnt(0)
	v_mfma_f32_32x32x16_f16 v[34:49], v[132:135], v[124:127], v[34:49]
	v_mfma_f32_32x32x16_f16 v[2:17], v[132:135], v[128:131], v[2:17]
	ds_read_b128 v[120:123], v96
	ds_read_b128 v[124:127], v113
	ds_read_b128 v[128:131], v113 offset:4096
	ds_read_b128 v[132:135], v112 offset:4096
	s_waitcnt lgkmcnt(2)
	v_mfma_f32_32x32x16_f16 v[50:65], v[120:123], v[124:127], v[50:65]
	s_waitcnt lgkmcnt(1)
	v_mfma_f32_32x32x16_f16 v[18:33], v[120:123], v[128:131], v[18:33]
	s_waitcnt lgkmcnt(0)
	v_mfma_f32_32x32x16_f16 v[34:49], v[132:135], v[124:127], v[34:49]
	v_mfma_f32_32x32x16_f16 v[2:17], v[132:135], v[128:131], v[2:17]
	ds_read_b128 v[120:123], v97
	ds_read_b128 v[124:127], v115
	ds_read_b128 v[128:131], v115 offset:4096
	ds_read_b128 v[132:135], v114 offset:4096
	buffer_load_dwordx4 v72, s[4:7], s43 offen lds
	s_mov_b32 m0, s36
	s_nop 0
	buffer_load_dwordx4 v74, s[4:7], s43 offen lds
	s_mov_b32 m0, s37
	s_waitcnt lgkmcnt(2)
	v_mfma_f32_32x32x16_f16 v[50:65], v[120:123], v[124:127], v[50:65]
	buffer_load_dwordx4 v73, s[12:15], s43 offen lds
	s_mov_b32 m0, s38
	s_nop 0
	buffer_load_dwordx4 v75, s[12:15], s43 offen lds
	s_waitcnt vmcnt(8)
	s_barrier
	s_add_i32 s43, s0, 0x780
	s_waitcnt lgkmcnt(1)
	v_mfma_f32_32x32x16_f16 v[18:33], v[120:123], v[128:131], v[18:33]
	s_mov_b32 m0, s39
	s_waitcnt lgkmcnt(0)
	v_mfma_f32_32x32x16_f16 v[34:49], v[132:135], v[124:127], v[34:49]
	v_mfma_f32_32x32x16_f16 v[2:17], v[132:135], v[128:131], v[2:17]
	ds_read_b128 v[120:123], v98
	ds_read_b128 v[124:127], v117
	ds_read_b128 v[128:131], v117 offset:4096
	ds_read_b128 v[132:135], v116 offset:4096
	s_waitcnt lgkmcnt(2)
	v_mfma_f32_32x32x16_f16 v[50:65], v[120:123], v[124:127], v[50:65]
	s_waitcnt lgkmcnt(1)
	v_mfma_f32_32x32x16_f16 v[18:33], v[120:123], v[128:131], v[18:33]
	s_waitcnt lgkmcnt(0)
	v_mfma_f32_32x32x16_f16 v[34:49], v[132:135], v[124:127], v[34:49]
	v_mfma_f32_32x32x16_f16 v[2:17], v[132:135], v[128:131], v[2:17]
	ds_read_b128 v[120:123], v99
	ds_read_b128 v[124:127], v119
	ds_read_b128 v[128:131], v119 offset:4096
	ds_read_b128 v[132:135], v118 offset:4096
	buffer_load_dwordx4 v72, s[4:7], s43 offen lds
	s_mov_b32 m0, s40
	s_nop 0
	buffer_load_dwordx4 v74, s[4:7], s43 offen lds
	s_mov_b32 m0, s41
	s_waitcnt lgkmcnt(2)
	v_mfma_f32_32x32x16_f16 v[50:65], v[120:123], v[124:127], v[50:65]
	buffer_load_dwordx4 v73, s[12:15], s43 offen lds
	s_mov_b32 m0, s42
	s_nop 0
	buffer_load_dwordx4 v75, s[12:15], s43 offen lds
	s_waitcnt vmcnt(8)
	s_barrier
	s_add_i32 s43, s0, 0x800
	s_waitcnt lgkmcnt(1)
	v_mfma_f32_32x32x16_f16 v[18:33], v[120:123], v[128:131], v[18:33]
	s_mov_b32 m0, s1
	s_waitcnt lgkmcnt(0)
	v_mfma_f32_32x32x16_f16 v[34:49], v[132:135], v[124:127], v[34:49]
	v_mfma_f32_32x32x16_f16 v[2:17], v[132:135], v[128:131], v[2:17]
	ds_read_b128 v[120:123], v110 offset:16384
	ds_read_b128 v[124:127], v111
	ds_read_b128 v[128:131], v111 offset:4096
	ds_read_b128 v[132:135], v110 offset:20480
	s_waitcnt lgkmcnt(2)
	v_mfma_f32_32x32x16_f16 v[50:65], v[120:123], v[124:127], v[50:65]
	s_waitcnt lgkmcnt(1)
	v_mfma_f32_32x32x16_f16 v[18:33], v[120:123], v[128:131], v[18:33]
	s_waitcnt lgkmcnt(0)
	v_mfma_f32_32x32x16_f16 v[34:49], v[132:135], v[124:127], v[34:49]
	v_mfma_f32_32x32x16_f16 v[2:17], v[132:135], v[128:131], v[2:17]
	ds_read_b128 v[120:123], v67 offset:16384
	ds_read_b128 v[124:127], v109
	ds_read_b128 v[128:131], v109 offset:4096
	ds_read_b128 v[132:135], v67 offset:20480
	buffer_load_dwordx4 v72, s[4:7], s43 offen lds
	s_mov_b32 m0, s2
	s_nop 0
	buffer_load_dwordx4 v74, s[4:7], s43 offen lds
	s_mov_b32 m0, s3
	s_waitcnt lgkmcnt(2)
	v_mfma_f32_32x32x16_f16 v[50:65], v[120:123], v[124:127], v[50:65]
	buffer_load_dwordx4 v73, s[12:15], s43 offen lds
	s_mov_b32 m0, s18
	s_nop 0
	buffer_load_dwordx4 v75, s[12:15], s43 offen lds
	s_waitcnt vmcnt(8)
	s_barrier
	s_add_i32 s43, s0, 0x880
	s_waitcnt lgkmcnt(1)
	v_mfma_f32_32x32x16_f16 v[18:33], v[120:123], v[128:131], v[18:33]
	s_mov_b32 m0, s19
	s_waitcnt lgkmcnt(0)
	v_mfma_f32_32x32x16_f16 v[34:49], v[132:135], v[124:127], v[34:49]
	v_mfma_f32_32x32x16_f16 v[2:17], v[132:135], v[128:131], v[2:17]
	ds_read_b128 v[120:123], v110 offset:49152
	ds_read_b128 v[124:127], v111 offset:32768
	ds_read_b128 v[128:131], v111 offset:36864
	ds_read_b128 v[132:135], v110 offset:53248
	s_waitcnt lgkmcnt(2)
	v_mfma_f32_32x32x16_f16 v[50:65], v[120:123], v[124:127], v[50:65]
	s_waitcnt lgkmcnt(1)
	v_mfma_f32_32x32x16_f16 v[18:33], v[120:123], v[128:131], v[18:33]
	s_waitcnt lgkmcnt(0)
	v_mfma_f32_32x32x16_f16 v[34:49], v[132:135], v[124:127], v[34:49]
	v_mfma_f32_32x32x16_f16 v[2:17], v[132:135], v[128:131], v[2:17]
	ds_read_b128 v[120:123], v67 offset:49152
	ds_read_b128 v[124:127], v109 offset:32768
	ds_read_b128 v[128:131], v109 offset:36864
	ds_read_b128 v[132:135], v67 offset:53248
	buffer_load_dwordx4 v72, s[4:7], s43 offen lds
	s_mov_b32 m0, s31
	s_nop 0
	buffer_load_dwordx4 v74, s[4:7], s43 offen lds
	s_mov_b32 m0, s33
	s_waitcnt lgkmcnt(2)
	v_mfma_f32_32x32x16_f16 v[50:65], v[120:123], v[124:127], v[50:65]
	buffer_load_dwordx4 v73, s[12:15], s43 offen lds
	s_mov_b32 m0, s34
	s_nop 0
	buffer_load_dwordx4 v75, s[12:15], s43 offen lds
	s_waitcnt vmcnt(8)
	s_barrier
	s_add_i32 s43, s0, 0x900
	s_waitcnt lgkmcnt(1)
	v_mfma_f32_32x32x16_f16 v[18:33], v[120:123], v[128:131], v[18:33]
	s_mov_b32 m0, s35
	s_waitcnt lgkmcnt(0)
	v_mfma_f32_32x32x16_f16 v[34:49], v[132:135], v[124:127], v[34:49]
	v_mfma_f32_32x32x16_f16 v[2:17], v[132:135], v[128:131], v[2:17]
	ds_read_b128 v[120:123], v96
	ds_read_b128 v[124:127], v113
	ds_read_b128 v[128:131], v113 offset:4096
	ds_read_b128 v[132:135], v112 offset:4096
	s_waitcnt lgkmcnt(2)
	v_mfma_f32_32x32x16_f16 v[50:65], v[120:123], v[124:127], v[50:65]
	s_waitcnt lgkmcnt(1)
	v_mfma_f32_32x32x16_f16 v[18:33], v[120:123], v[128:131], v[18:33]
	s_waitcnt lgkmcnt(0)
	v_mfma_f32_32x32x16_f16 v[34:49], v[132:135], v[124:127], v[34:49]
	v_mfma_f32_32x32x16_f16 v[2:17], v[132:135], v[128:131], v[2:17]
	ds_read_b128 v[120:123], v97
	ds_read_b128 v[124:127], v115
	ds_read_b128 v[128:131], v115 offset:4096
	ds_read_b128 v[132:135], v114 offset:4096
	buffer_load_dwordx4 v72, s[4:7], s43 offen lds
	s_mov_b32 m0, s36
	s_nop 0
	buffer_load_dwordx4 v74, s[4:7], s43 offen lds
	s_mov_b32 m0, s37
	s_waitcnt lgkmcnt(2)
	v_mfma_f32_32x32x16_f16 v[50:65], v[120:123], v[124:127], v[50:65]
	buffer_load_dwordx4 v73, s[12:15], s43 offen lds
	s_mov_b32 m0, s38
	s_nop 0
	buffer_load_dwordx4 v75, s[12:15], s43 offen lds
	s_waitcnt vmcnt(8)
	s_barrier
	s_add_i32 s43, s0, 0x980
	s_waitcnt lgkmcnt(1)
	v_mfma_f32_32x32x16_f16 v[18:33], v[120:123], v[128:131], v[18:33]
	s_mov_b32 m0, s39
	s_waitcnt lgkmcnt(0)
	v_mfma_f32_32x32x16_f16 v[34:49], v[132:135], v[124:127], v[34:49]
	v_mfma_f32_32x32x16_f16 v[2:17], v[132:135], v[128:131], v[2:17]
	ds_read_b128 v[120:123], v98
	ds_read_b128 v[124:127], v117
	ds_read_b128 v[128:131], v117 offset:4096
	ds_read_b128 v[132:135], v116 offset:4096
	s_waitcnt lgkmcnt(2)
	v_mfma_f32_32x32x16_f16 v[50:65], v[120:123], v[124:127], v[50:65]
	s_waitcnt lgkmcnt(1)
	v_mfma_f32_32x32x16_f16 v[18:33], v[120:123], v[128:131], v[18:33]
	s_waitcnt lgkmcnt(0)
	v_mfma_f32_32x32x16_f16 v[34:49], v[132:135], v[124:127], v[34:49]
	v_mfma_f32_32x32x16_f16 v[2:17], v[132:135], v[128:131], v[2:17]
	ds_read_b128 v[120:123], v99
	ds_read_b128 v[124:127], v119
	ds_read_b128 v[128:131], v119 offset:4096
	ds_read_b128 v[132:135], v118 offset:4096
	buffer_load_dwordx4 v72, s[4:7], s43 offen lds
	s_mov_b32 m0, s40
	s_nop 0
	buffer_load_dwordx4 v74, s[4:7], s43 offen lds
	s_mov_b32 m0, s41
	s_waitcnt lgkmcnt(2)
	v_mfma_f32_32x32x16_f16 v[50:65], v[120:123], v[124:127], v[50:65]
	buffer_load_dwordx4 v73, s[12:15], s43 offen lds
	s_mov_b32 m0, s42
	s_nop 0
	buffer_load_dwordx4 v75, s[12:15], s43 offen lds
	s_waitcnt vmcnt(8)
	s_barrier
	s_add_i32 s43, s0, 0xa00
	s_waitcnt lgkmcnt(1)
	v_mfma_f32_32x32x16_f16 v[18:33], v[120:123], v[128:131], v[18:33]
	s_mov_b32 m0, s1
	s_waitcnt lgkmcnt(0)
	v_mfma_f32_32x32x16_f16 v[34:49], v[132:135], v[124:127], v[34:49]
	v_mfma_f32_32x32x16_f16 v[2:17], v[132:135], v[128:131], v[2:17]
	ds_read_b128 v[120:123], v110 offset:16384
	ds_read_b128 v[124:127], v111
	ds_read_b128 v[128:131], v111 offset:4096
	ds_read_b128 v[132:135], v110 offset:20480
	s_waitcnt lgkmcnt(2)
	v_mfma_f32_32x32x16_f16 v[50:65], v[120:123], v[124:127], v[50:65]
	s_waitcnt lgkmcnt(1)
	v_mfma_f32_32x32x16_f16 v[18:33], v[120:123], v[128:131], v[18:33]
	s_waitcnt lgkmcnt(0)
	v_mfma_f32_32x32x16_f16 v[34:49], v[132:135], v[124:127], v[34:49]
	v_mfma_f32_32x32x16_f16 v[2:17], v[132:135], v[128:131], v[2:17]
	ds_read_b128 v[120:123], v67 offset:16384
	ds_read_b128 v[124:127], v109
	ds_read_b128 v[128:131], v109 offset:4096
	ds_read_b128 v[132:135], v67 offset:20480
	buffer_load_dwordx4 v72, s[4:7], s43 offen lds
	s_mov_b32 m0, s2
	s_nop 0
	buffer_load_dwordx4 v74, s[4:7], s43 offen lds
	s_mov_b32 m0, s3
	s_waitcnt lgkmcnt(2)
	v_mfma_f32_32x32x16_f16 v[50:65], v[120:123], v[124:127], v[50:65]
	buffer_load_dwordx4 v73, s[12:15], s43 offen lds
	s_mov_b32 m0, s18
	s_nop 0
	buffer_load_dwordx4 v75, s[12:15], s43 offen lds
	s_waitcnt vmcnt(8)
	s_barrier
	s_add_i32 s43, s0, 0xa80
	s_waitcnt lgkmcnt(1)
	v_mfma_f32_32x32x16_f16 v[18:33], v[120:123], v[128:131], v[18:33]
	s_mov_b32 m0, s19
	s_waitcnt lgkmcnt(0)
	v_mfma_f32_32x32x16_f16 v[34:49], v[132:135], v[124:127], v[34:49]
	v_mfma_f32_32x32x16_f16 v[2:17], v[132:135], v[128:131], v[2:17]
	ds_read_b128 v[120:123], v110 offset:49152
	ds_read_b128 v[124:127], v111 offset:32768
	ds_read_b128 v[128:131], v111 offset:36864
	ds_read_b128 v[132:135], v110 offset:53248
	s_waitcnt lgkmcnt(2)
	v_mfma_f32_32x32x16_f16 v[50:65], v[120:123], v[124:127], v[50:65]
	s_waitcnt lgkmcnt(1)
	v_mfma_f32_32x32x16_f16 v[18:33], v[120:123], v[128:131], v[18:33]
	s_waitcnt lgkmcnt(0)
	v_mfma_f32_32x32x16_f16 v[34:49], v[132:135], v[124:127], v[34:49]
	v_mfma_f32_32x32x16_f16 v[2:17], v[132:135], v[128:131], v[2:17]
	ds_read_b128 v[120:123], v67 offset:49152
	ds_read_b128 v[124:127], v109 offset:32768
	ds_read_b128 v[128:131], v109 offset:36864
	ds_read_b128 v[132:135], v67 offset:53248
	buffer_load_dwordx4 v72, s[4:7], s43 offen lds
	s_mov_b32 m0, s31
	s_nop 0
	buffer_load_dwordx4 v74, s[4:7], s43 offen lds
	s_mov_b32 m0, s33
	s_waitcnt lgkmcnt(2)
	v_mfma_f32_32x32x16_f16 v[50:65], v[120:123], v[124:127], v[50:65]
	buffer_load_dwordx4 v73, s[12:15], s43 offen lds
	s_mov_b32 m0, s34
	s_nop 0
	buffer_load_dwordx4 v75, s[12:15], s43 offen lds
	s_waitcnt vmcnt(8)
	s_barrier
	s_add_i32 s43, s0, 0xb00
	s_waitcnt lgkmcnt(1)
	v_mfma_f32_32x32x16_f16 v[18:33], v[120:123], v[128:131], v[18:33]
	s_mov_b32 m0, s35
	s_waitcnt lgkmcnt(0)
	v_mfma_f32_32x32x16_f16 v[34:49], v[132:135], v[124:127], v[34:49]
	v_mfma_f32_32x32x16_f16 v[2:17], v[132:135], v[128:131], v[2:17]
	ds_read_b128 v[120:123], v96
	ds_read_b128 v[124:127], v113
	ds_read_b128 v[128:131], v113 offset:4096
	ds_read_b128 v[132:135], v112 offset:4096
	s_waitcnt lgkmcnt(2)
	v_mfma_f32_32x32x16_f16 v[50:65], v[120:123], v[124:127], v[50:65]
	s_waitcnt lgkmcnt(1)
	v_mfma_f32_32x32x16_f16 v[18:33], v[120:123], v[128:131], v[18:33]
	s_waitcnt lgkmcnt(0)
	v_mfma_f32_32x32x16_f16 v[34:49], v[132:135], v[124:127], v[34:49]
	v_mfma_f32_32x32x16_f16 v[2:17], v[132:135], v[128:131], v[2:17]
	ds_read_b128 v[120:123], v97
	ds_read_b128 v[124:127], v115
	ds_read_b128 v[128:131], v115 offset:4096
	ds_read_b128 v[132:135], v114 offset:4096
	buffer_load_dwordx4 v72, s[4:7], s43 offen lds
	s_mov_b32 m0, s36
	s_nop 0
	buffer_load_dwordx4 v74, s[4:7], s43 offen lds
	s_mov_b32 m0, s37
	s_waitcnt lgkmcnt(2)
	v_mfma_f32_32x32x16_f16 v[50:65], v[120:123], v[124:127], v[50:65]
	buffer_load_dwordx4 v73, s[12:15], s43 offen lds
	s_mov_b32 m0, s38
	s_nop 0
	buffer_load_dwordx4 v75, s[12:15], s43 offen lds
	s_waitcnt vmcnt(8)
	s_barrier
	s_add_i32 s43, s0, 0xb80
	s_waitcnt lgkmcnt(1)
	v_mfma_f32_32x32x16_f16 v[18:33], v[120:123], v[128:131], v[18:33]
	s_mov_b32 m0, s39
	s_waitcnt lgkmcnt(0)
	v_mfma_f32_32x32x16_f16 v[34:49], v[132:135], v[124:127], v[34:49]
	v_mfma_f32_32x32x16_f16 v[2:17], v[132:135], v[128:131], v[2:17]
	ds_read_b128 v[120:123], v98
	ds_read_b128 v[124:127], v117
	ds_read_b128 v[128:131], v117 offset:4096
	ds_read_b128 v[132:135], v116 offset:4096
	s_waitcnt lgkmcnt(2)
	v_mfma_f32_32x32x16_f16 v[50:65], v[120:123], v[124:127], v[50:65]
	s_waitcnt lgkmcnt(1)
	v_mfma_f32_32x32x16_f16 v[18:33], v[120:123], v[128:131], v[18:33]
	s_waitcnt lgkmcnt(0)
	v_mfma_f32_32x32x16_f16 v[34:49], v[132:135], v[124:127], v[34:49]
	v_mfma_f32_32x32x16_f16 v[2:17], v[132:135], v[128:131], v[2:17]
	ds_read_b128 v[120:123], v99
	ds_read_b128 v[124:127], v119
	ds_read_b128 v[128:131], v119 offset:4096
	ds_read_b128 v[132:135], v118 offset:4096
	buffer_load_dwordx4 v72, s[4:7], s43 offen lds
	s_mov_b32 m0, s40
	s_nop 0
	buffer_load_dwordx4 v74, s[4:7], s43 offen lds
	s_mov_b32 m0, s41
	s_waitcnt lgkmcnt(2)
	v_mfma_f32_32x32x16_f16 v[50:65], v[120:123], v[124:127], v[50:65]
	buffer_load_dwordx4 v73, s[12:15], s43 offen lds
	s_mov_b32 m0, s42
	s_nop 0
	buffer_load_dwordx4 v75, s[12:15], s43 offen lds
	s_waitcnt vmcnt(8)
	s_barrier
	s_add_i32 s43, s0, 0xc00
	s_waitcnt lgkmcnt(1)
	v_mfma_f32_32x32x16_f16 v[18:33], v[120:123], v[128:131], v[18:33]
	s_mov_b32 m0, s1
	s_waitcnt lgkmcnt(0)
	v_mfma_f32_32x32x16_f16 v[34:49], v[132:135], v[124:127], v[34:49]
	v_mfma_f32_32x32x16_f16 v[2:17], v[132:135], v[128:131], v[2:17]
	ds_read_b128 v[120:123], v110 offset:16384
	ds_read_b128 v[124:127], v111
	ds_read_b128 v[128:131], v111 offset:4096
	ds_read_b128 v[132:135], v110 offset:20480
	s_waitcnt lgkmcnt(2)
	v_mfma_f32_32x32x16_f16 v[50:65], v[120:123], v[124:127], v[50:65]
	s_waitcnt lgkmcnt(1)
	v_mfma_f32_32x32x16_f16 v[18:33], v[120:123], v[128:131], v[18:33]
	s_waitcnt lgkmcnt(0)
	v_mfma_f32_32x32x16_f16 v[34:49], v[132:135], v[124:127], v[34:49]
	v_mfma_f32_32x32x16_f16 v[2:17], v[132:135], v[128:131], v[2:17]
	ds_read_b128 v[120:123], v67 offset:16384
	ds_read_b128 v[124:127], v109
	ds_read_b128 v[128:131], v109 offset:4096
	ds_read_b128 v[132:135], v67 offset:20480
	buffer_load_dwordx4 v72, s[4:7], s43 offen lds
	s_mov_b32 m0, s2
	s_nop 0
	buffer_load_dwordx4 v74, s[4:7], s43 offen lds
	s_mov_b32 m0, s3
	s_waitcnt lgkmcnt(2)
	v_mfma_f32_32x32x16_f16 v[50:65], v[120:123], v[124:127], v[50:65]
	buffer_load_dwordx4 v73, s[12:15], s43 offen lds
	s_mov_b32 m0, s18
	s_nop 0
	buffer_load_dwordx4 v75, s[12:15], s43 offen lds
	s_waitcnt vmcnt(8)
	s_barrier
	s_add_i32 s43, s0, 0xc80
	s_waitcnt lgkmcnt(1)
	v_mfma_f32_32x32x16_f16 v[18:33], v[120:123], v[128:131], v[18:33]
	s_mov_b32 m0, s19
	s_add_i32 s19, s0, 0xd00
	s_waitcnt lgkmcnt(0)
	v_mfma_f32_32x32x16_f16 v[34:49], v[132:135], v[124:127], v[34:49]
	v_mfma_f32_32x32x16_f16 v[2:17], v[132:135], v[128:131], v[2:17]
	ds_read_b128 v[120:123], v110 offset:49152
	ds_read_b128 v[124:127], v111 offset:32768
	ds_read_b128 v[128:131], v111 offset:36864
	ds_read_b128 v[132:135], v110 offset:53248
	s_waitcnt lgkmcnt(2)
	v_mfma_f32_32x32x16_f16 v[50:65], v[120:123], v[124:127], v[50:65]
	s_waitcnt lgkmcnt(1)
	v_mfma_f32_32x32x16_f16 v[18:33], v[120:123], v[128:131], v[18:33]
	s_waitcnt lgkmcnt(0)
	v_mfma_f32_32x32x16_f16 v[34:49], v[132:135], v[124:127], v[34:49]
	v_mfma_f32_32x32x16_f16 v[2:17], v[132:135], v[128:131], v[2:17]
	ds_read_b128 v[120:123], v67 offset:49152
	ds_read_b128 v[124:127], v109 offset:32768
	ds_read_b128 v[128:131], v109 offset:36864
	ds_read_b128 v[132:135], v67 offset:53248
	buffer_load_dwordx4 v72, s[4:7], s43 offen lds
	s_mov_b32 m0, s31
	s_add_i32 s31, s0, 0xe00
	buffer_load_dwordx4 v74, s[4:7], s43 offen lds
	s_mov_b32 m0, s33
	s_waitcnt lgkmcnt(2)
	v_mfma_f32_32x32x16_f16 v[50:65], v[120:123], v[124:127], v[50:65]
	buffer_load_dwordx4 v73, s[12:15], s43 offen lds
	s_mov_b32 m0, s34
	s_nop 0
	buffer_load_dwordx4 v75, s[12:15], s43 offen lds
	s_waitcnt vmcnt(8)
	s_barrier
	s_mov_b32 m0, s35
	s_waitcnt lgkmcnt(1)
	v_mfma_f32_32x32x16_f16 v[18:33], v[120:123], v[128:131], v[18:33]
	s_waitcnt lgkmcnt(0)
	v_mfma_f32_32x32x16_f16 v[34:49], v[132:135], v[124:127], v[34:49]
	v_mfma_f32_32x32x16_f16 v[2:17], v[132:135], v[128:131], v[2:17]
	ds_read_b128 v[120:123], v96
	ds_read_b128 v[124:127], v113
	ds_read_b128 v[128:131], v113 offset:4096
	ds_read_b128 v[132:135], v112 offset:4096
	s_waitcnt lgkmcnt(2)
	v_mfma_f32_32x32x16_f16 v[50:65], v[120:123], v[124:127], v[50:65]
	s_waitcnt lgkmcnt(1)
	v_mfma_f32_32x32x16_f16 v[18:33], v[120:123], v[128:131], v[18:33]
	s_waitcnt lgkmcnt(0)
	v_mfma_f32_32x32x16_f16 v[34:49], v[132:135], v[124:127], v[34:49]
	v_mfma_f32_32x32x16_f16 v[2:17], v[132:135], v[128:131], v[2:17]
	ds_read_b128 v[120:123], v97
	ds_read_b128 v[124:127], v115
	ds_read_b128 v[128:131], v115 offset:4096
	ds_read_b128 v[132:135], v114 offset:4096
	buffer_load_dwordx4 v72, s[4:7], s19 offen lds
	s_mov_b32 m0, s36
	s_nop 0
	buffer_load_dwordx4 v74, s[4:7], s19 offen lds
	s_mov_b32 m0, s37
	s_waitcnt lgkmcnt(2)
	v_mfma_f32_32x32x16_f16 v[50:65], v[120:123], v[124:127], v[50:65]
	buffer_load_dwordx4 v73, s[12:15], s19 offen lds
	s_mov_b32 m0, s38
	s_nop 0
	buffer_load_dwordx4 v75, s[12:15], s19 offen lds
	s_waitcnt vmcnt(8)
	s_barrier
	s_add_i32 s19, s0, 0xd80
	s_waitcnt lgkmcnt(1)
	v_mfma_f32_32x32x16_f16 v[18:33], v[120:123], v[128:131], v[18:33]
	s_mov_b32 m0, s39
	s_ashr_i32 s0, s23, 31
	s_xor_b32 s0, s0, s25
	s_waitcnt lgkmcnt(0)
	v_mfma_f32_32x32x16_f16 v[34:49], v[132:135], v[124:127], v[34:49]
	v_mfma_f32_32x32x16_f16 v[2:17], v[132:135], v[128:131], v[2:17]
	ds_read_b128 v[120:123], v98
	ds_read_b128 v[124:127], v117
	ds_read_b128 v[128:131], v117 offset:4096
	ds_read_b128 v[132:135], v116 offset:4096
	s_waitcnt lgkmcnt(2)
	v_mfma_f32_32x32x16_f16 v[50:65], v[120:123], v[124:127], v[50:65]
	s_waitcnt lgkmcnt(1)
	v_mfma_f32_32x32x16_f16 v[18:33], v[120:123], v[128:131], v[18:33]
	s_waitcnt lgkmcnt(0)
	v_mfma_f32_32x32x16_f16 v[34:49], v[132:135], v[124:127], v[34:49]
	v_mfma_f32_32x32x16_f16 v[2:17], v[132:135], v[128:131], v[2:17]
	ds_read_b128 v[120:123], v99
	ds_read_b128 v[124:127], v119
	ds_read_b128 v[128:131], v119 offset:4096
	ds_read_b128 v[132:135], v118 offset:4096
	buffer_load_dwordx4 v72, s[4:7], s19 offen lds
	s_mov_b32 m0, s40
	s_nop 0
	buffer_load_dwordx4 v74, s[4:7], s19 offen lds
	s_mov_b32 m0, s41
	s_waitcnt lgkmcnt(2)
	v_mfma_f32_32x32x16_f16 v[50:65], v[120:123], v[124:127], v[50:65]
	buffer_load_dwordx4 v73, s[12:15], s19 offen lds
	s_mov_b32 m0, s42
	s_nop 0
	buffer_load_dwordx4 v75, s[12:15], s19 offen lds
	s_waitcnt vmcnt(8)
	s_barrier
	s_mov_b32 m0, s1
	s_waitcnt lgkmcnt(1)
	v_mfma_f32_32x32x16_f16 v[18:33], v[120:123], v[128:131], v[18:33]
	s_abs_i32 s1, s23
	s_waitcnt lgkmcnt(0)
	v_mfma_f32_32x32x16_f16 v[34:49], v[132:135], v[124:127], v[34:49]
	v_mfma_f32_32x32x16_f16 v[2:17], v[132:135], v[128:131], v[2:17]
	ds_read_b128 v[120:123], v110 offset:16384
	ds_read_b128 v[124:127], v111
	ds_read_b128 v[128:131], v111 offset:4096
	ds_read_b128 v[132:135], v110 offset:20480
	s_waitcnt lgkmcnt(2)
	v_mfma_f32_32x32x16_f16 v[50:65], v[120:123], v[124:127], v[50:65]
	s_waitcnt lgkmcnt(1)
	v_mfma_f32_32x32x16_f16 v[18:33], v[120:123], v[128:131], v[18:33]
	s_waitcnt lgkmcnt(0)
	v_mfma_f32_32x32x16_f16 v[34:49], v[132:135], v[124:127], v[34:49]
	v_mfma_f32_32x32x16_f16 v[2:17], v[132:135], v[128:131], v[2:17]
	ds_read_b128 v[120:123], v67 offset:16384
	ds_read_b128 v[124:127], v109
	ds_read_b128 v[128:131], v109 offset:4096
	ds_read_b128 v[132:135], v67 offset:20480
	buffer_load_dwordx4 v72, s[4:7], s31 offen lds
	s_mov_b32 m0, s2
	s_mul_hi_u32 s2, s1, s26
	buffer_load_dwordx4 v74, s[4:7], s31 offen lds
	s_mov_b32 m0, s3
	s_mul_i32 s3, s2, s24
	s_waitcnt lgkmcnt(2)
	v_mfma_f32_32x32x16_f16 v[50:65], v[120:123], v[124:127], v[50:65]
	buffer_load_dwordx4 v73, s[12:15], s31 offen lds
	s_mov_b32 m0, s18
	s_sub_i32 s1, s1, s3
	buffer_load_dwordx4 v75, s[12:15], s31 offen lds
	s_waitcnt vmcnt(8)
	s_barrier
	s_add_i32 s3, s2, 1
	s_waitcnt lgkmcnt(1)
	v_mfma_f32_32x32x16_f16 v[18:33], v[120:123], v[128:131], v[18:33]
	s_sub_i32 s14, s1, s24
	s_cmp_ge_u32 s1, s24
	s_cselect_b32 s2, s3, s2
	s_cselect_b32 s1, s14, s1
	s_add_i32 s3, s2, 1
	s_cmp_ge_u32 s1, s24
	s_cselect_b32 s1, s3, s2
	s_waitcnt lgkmcnt(0)
	v_mfma_f32_32x32x16_f16 v[34:49], v[132:135], v[124:127], v[34:49]
	s_xor_b32 s1, s1, s0
	s_sub_i32 s0, s1, s0
	s_mul_i32 s1, s0, s21
	s_sub_i32 s15, s23, s1
	s_lshl_b32 s2, s15, 7
	s_lshl_b32 s14, s0, 7
	s_ashr_i32 s3, s2, 31
	v_mfma_f32_32x32x16_f16 v[2:17], v[132:135], v[128:131], v[2:17]
	ds_read_b128 v[120:123], v110 offset:49152
	ds_read_b128 v[124:127], v111 offset:32768
	ds_read_b128 v[128:131], v111 offset:36864
	ds_read_b128 v[132:135], v110 offset:53248
	s_waitcnt lgkmcnt(2)
	v_mfma_f32_32x32x16_f16 v[50:65], v[120:123], v[124:127], v[50:65]
	s_waitcnt lgkmcnt(1)
	v_mfma_f32_32x32x16_f16 v[18:33], v[120:123], v[128:131], v[18:33]
	s_waitcnt lgkmcnt(0)
	v_mfma_f32_32x32x16_f16 v[34:49], v[132:135], v[124:127], v[34:49]
	v_mfma_f32_32x32x16_f16 v[2:17], v[132:135], v[128:131], v[2:17]
	ds_read_b128 v[120:123], v67 offset:49152
	ds_read_b128 v[124:127], v109 offset:32768
	ds_read_b128 v[128:131], v109 offset:36864
	ds_read_b128 v[132:135], v67 offset:53248
	s_waitcnt vmcnt(4)
	s_barrier
	s_waitcnt lgkmcnt(2)
	v_mfma_f32_32x32x16_f16 v[50:65], v[120:123], v[124:127], v[50:65]
	s_waitcnt lgkmcnt(1)
	v_mfma_f32_32x32x16_f16 v[18:33], v[120:123], v[128:131], v[18:33]
	s_waitcnt lgkmcnt(0)
	v_mfma_f32_32x32x16_f16 v[34:49], v[132:135], v[124:127], v[34:49]
	v_mfma_f32_32x32x16_f16 v[2:17], v[132:135], v[128:131], v[2:17]
	ds_read_b128 v[120:123], v96
	ds_read_b128 v[124:127], v113
	ds_read_b128 v[128:131], v113 offset:4096
	ds_read_b128 v[110:113], v112 offset:4096
	s_waitcnt lgkmcnt(2)
	v_mfma_f32_32x32x16_f16 v[50:65], v[120:123], v[124:127], v[50:65]
	s_waitcnt lgkmcnt(1)
	v_mfma_f32_32x32x16_f16 v[18:33], v[120:123], v[128:131], v[18:33]
	s_waitcnt lgkmcnt(0)
	v_mfma_f32_32x32x16_f16 v[34:49], v[110:113], v[124:127], v[34:49]
	ds_read_b128 v[120:123], v97
	ds_read_b128 v[124:127], v115
	ds_read_b128 v[132:135], v115 offset:4096
	s_waitcnt lgkmcnt(1)
	v_mfma_f32_32x32x16_f16 v[50:65], v[120:123], v[124:127], v[50:65]
	s_waitcnt lgkmcnt(0)
	v_mfma_f32_32x32x16_f16 v[18:33], v[120:123], v[132:135], v[18:33]
	ds_read_b128 v[120:123], v114 offset:4096
	s_waitcnt vmcnt(0)
	s_barrier
	v_mfma_f32_32x32x16_f16 v[2:17], v[110:113], v[128:131], v[2:17]
	s_waitcnt lgkmcnt(0)
	v_mfma_f32_32x32x16_f16 v[34:49], v[120:123], v[124:127], v[34:49]
	ds_read_b128 v[124:127], v98
	ds_read_b128 v[136:139], v117
	ds_read_b128 v[140:143], v117 offset:4096
	ds_read_b128 v[114:117], v116 offset:4096
	s_waitcnt lgkmcnt(2)
	v_mfma_f32_32x32x16_f16 v[50:65], v[124:127], v[136:139], v[50:65]
	s_waitcnt lgkmcnt(1)
	v_mfma_f32_32x32x16_f16 v[18:33], v[124:127], v[140:143], v[18:33]
	v_mfma_f32_32x32x16_f16 v[2:17], v[120:123], v[132:135], v[2:17]
	s_waitcnt lgkmcnt(0)
	v_mfma_f32_32x32x16_f16 v[34:49], v[114:117], v[136:139], v[34:49]
	ds_read_b128 v[124:127], v99
	ds_read_b128 v[136:139], v119
	ds_read_b128 v[144:147], v119 offset:4096
	s_waitcnt lgkmcnt(1)
	v_mfma_f32_32x32x16_f16 v[50:65], v[124:127], v[136:139], v[50:65]
	s_waitcnt lgkmcnt(0)
	v_mfma_f32_32x32x16_f16 v[18:33], v[124:127], v[144:147], v[18:33]
	ds_read_b128 v[124:127], v118 offset:4096
	s_waitcnt lgkmcnt(0)
	s_barrier
	s_nop 8
	ds_write_b128 v100, v[50:53]
	ds_write_b128 v101, v[54:57]
	v_mfma_f32_32x32x16_f16 v[2:17], v[114:117], v[140:143], v[2:17]
	s_waitcnt lgkmcnt(2)
	v_mfma_f32_32x32x16_f16 v[2:17], v[124:127], v[144:147], v[2:17]
	v_mfma_f32_32x32x16_f16 v[34:49], v[124:127], v[136:139], v[34:49]
	ds_write_b128 v102, v[58:61]
	ds_write_b128 v103, v[62:65]
	s_nop 9
	ds_write_b128 v104, v[34:37]
	ds_write_b128 v105, v[38:41]
	ds_write_b128 v106, v[42:45]
	ds_write_b128 v107, v[46:49]
	ds_write_b128 v100, v[18:21] offset:16384
	ds_write_b128 v101, v[22:25] offset:16384
	ds_write_b128 v102, v[26:29] offset:16384
	ds_write_b128 v103, v[30:33] offset:16384
	ds_write_b128 v104, v[2:5] offset:16384
	ds_write_b128 v105, v[6:9] offset:16384
	ds_write_b128 v106, v[10:13] offset:16384
	ds_write_b128 v107, v[14:17] offset:16384
	v_or_b32_e32 v25, s14, v1
	s_waitcnt lgkmcnt(0)
	s_barrier
	v_mov_b64_e32 v[10:11], v[160:161]
	v_mov_b64_e32 v[12:13], v[162:163]
	v_mov_b64_e32 v[6:7], v[176:177]
	v_mov_b64_e32 v[8:9], v[178:179]
	v_mov_b64_e32 v[2:3], v[180:181]
	v_mov_b64_e32 v[4:5], v[182:183]
	v_add_u32_e32 v14, 0, v85
	v_add_u32_e32 v18, s28, v85
	ds_read_b128 v[14:17], v14
	ds_read_b128 v[26:29], v18
	v_mov_b64_e32 v[18:19], v[164:165]
	v_mov_b64_e32 v[20:21], v[166:167]
	s_waitcnt lgkmcnt(0)
	v_pk_add_f32 v[16:17], v[16:17], v[28:29]
	v_add_f32_e32 v35, v14, v26
	v_mov_b32_e32 v34, v27
	v_cvt_f32_f16_e32 v30, v11
	v_cvt_f32_f16_sdwa v31, v11 dst_sel:DWORD dst_unused:UNUSED_PAD src0_sel:WORD_1
	v_add_u32_e32 v11, 0, v86
	v_pk_add_f32 v[16:17], v[8:9], v[16:17]
	ds_read_b128 v[26:29], v11
	v_add_u32_e32 v11, s28, v86
	v_pk_add_f32 v[36:37], v[16:17], v[30:31]
	ds_read_b128 v[30:33], v11
	v_cvt_f32_f16_e32 v38, v13
	v_cvt_f32_f16_sdwa v39, v13 dst_sel:DWORD dst_unused:UNUSED_PAD src0_sel:WORD_1
	v_mov_b32_e32 v16, v2
	v_mov_b32_e32 v17, v3
	s_waitcnt lgkmcnt(0)
	v_pk_add_f32 v[28:29], v[28:29], v[32:33]
	v_cvt_f32_f16_e32 v32, v10
	v_pk_add_f32 v[28:29], v[4:5], v[28:29]
	v_pk_mov_b32 v[16:17], v[26:27], v[16:17] op_sel:[1,0]
	v_pk_add_f32 v[28:29], v[28:29], v[38:39]
	v_cvt_f32_f16_e32 v38, v12
	v_add_f32_e32 v26, v26, v30
	v_cvt_f32_f16_sdwa v33, v10 dst_sel:DWORD dst_unused:UNUSED_PAD src0_sel:WORD_1
	v_cvt_f32_f16_sdwa v30, v12 dst_sel:DWORD dst_unused:UNUSED_PAD src0_sel:WORD_1
	v_pk_mov_b32 v[14:15], v[14:15], v[6:7] op_sel:[1,0]
	v_mov_b32_e32 v10, v31
	v_mov_b32_e32 v11, v26
	v_pk_add_f32 v[44:45], v[14:15], v[34:35]
	v_mov_b32_e32 v12, v7
	v_mov_b32_e32 v13, v32
	v_pk_add_f32 v[10:11], v[16:17], v[10:11]
	v_pk_add_f32 v[46:47], v[12:13], v[44:45]
	v_mov_b32_e32 v22, v3
	v_mov_b32_e32 v23, v38
	v_pk_add_f32 v[48:49], v[22:23], v[10:11]
	v_mov_b32_e32 v10, v33
	v_mov_b32_e32 v11, v47
	v_pk_add_f32 v[50:51], v[46:47], v[10:11]
	v_mov_b64_e32 v[14:15], v[168:169]
	v_mov_b64_e32 v[16:17], v[170:171]
	v_mov_b64_e32 v[10:11], v[172:173]
	v_mov_b64_e32 v[12:13], v[174:175]
	v_mov_b32_e32 v31, v49
	v_pk_add_f32 v[40:41], v[48:49], v[30:31]
	v_pk_mov_b32 v[30:31], v[34:35], v[44:45] op_sel:[1,0]
	v_mov_b32_e32 v27, v44
	v_mov_b32_e32 v3, v7
	v_pk_add_f32 v[30:31], v[6:7], v[30:31]
	v_mov_b32_e32 v39, v33
	v_pk_add_f32 v[26:27], v[2:3], v[26:27]
	v_pk_add_f32 v[30:31], v[30:31], v[32:33]
	v_pk_add_f32 v[26:27], v[26:27], v[38:39]
	v_pk_mul_f32 v[32:33], v[46:47], v[46:47]
	v_pk_add_f32 v[34:35], v[30:31], v[26:27]
	v_pk_mul_f32 v[26:27], v[30:31], v[26:27]
	v_mov_b32_e32 v51, v33
	v_pk_mul_f32 v[32:33], v[48:49], v[48:49]
	v_mov_b32_e32 v35, v27
	v_pk_mul_f32 v[26:27], v[40:41], v[40:41]
	v_mov_b32_e32 v32, v40
	v_mov_b32_e32 v67, v26
	v_pk_add_f32 v[32:33], v[50:51], v[32:33]
	v_pk_add_f32 v[26:27], v[34:35], v[66:67]
	v_pk_mul_f32 v[30:31], v[36:37], v[36:37]
	v_pk_mul_f32 v[34:35], v[28:29], v[28:29]
	v_pk_add_f32 v[26:27], v[32:33], v[26:27]
	v_mov_b32_e32 v32, v36
	v_mov_b32_e32 v33, v30
	v_mov_b32_e32 v38, v28
	v_mov_b32_e32 v39, v34
	v_pk_add_f32 v[32:33], v[32:33], v[38:39]
	v_mov_b32_e32 v30, v37
	v_mov_b32_e32 v34, v29
	v_pk_add_f32 v[26:27], v[26:27], v[32:33]
	v_pk_add_f32 v[30:31], v[30:31], v[34:35]
	v_pk_add_f32 v[26:27], v[26:27], v[30:31]
	s_nop 1
	v_mov_b32_dpp v32, v26 row_mirror row_mask:0xf bank_mask:0xf
	v_mov_b32_dpp v33, v27 row_mirror row_mask:0xf bank_mask:0xf
	v_cvt_pk_f16_f32 v39, v28, v29
	v_cvt_pk_f16_f32 v37, v36, v37
	s_waitcnt lgkmcnt(0)
	v_pk_add_f32 v[26:27], v[26:27], v[32:33]
	s_nop 1
	v_mov_b32_dpp v32, v26 row_half_mirror row_mask:0xf bank_mask:0xf
	v_mov_b32_dpp v33, v27 row_half_mirror row_mask:0xf bank_mask:0xf
	v_cvt_pk_f16_f32 v36, v47, v50
	v_cvt_pk_f16_f32 v38, v49, v40
	s_waitcnt lgkmcnt(0)
	v_pk_add_f32 v[26:27], v[26:27], v[32:33]
	s_nop 1
	v_mov_b32_dpp v28, v26 quad_perm:[2,3,0,1] row_mask:0xf bank_mask:0xf
	v_mov_b32_dpp v29, v27 quad_perm:[2,3,0,1] row_mask:0xf bank_mask:0xf
	v_or_b32_e32 v32, s2, v78
	v_mul_lo_u32 v24, v25, s30
	v_add_lshl_u32 v24, v32, v24, 1
	buffer_store_dwordx4 v[36:39], v24, s[8:11], 0 offen sc1
	s_waitcnt lgkmcnt(0)
	v_pk_add_f32 v[26:27], v[26:27], v[28:29]
	s_lshl_b32 s2, s15, 4
	v_mov_b32_e32 v24, v7
	s_nop 1
	v_mov_b32_dpp v28, v26 quad_perm:[1,0,3,2] row_mask:0xf bank_mask:0xf
	v_mov_b32_dpp v29, v27 quad_perm:[1,0,3,2] row_mask:0xf bank_mask:0xf
	s_and_saveexec_b64 s[0:1], vcc
	s_cbranch_execz .LBB9_5
	s_waitcnt lgkmcnt(0)
	v_pk_add_f32 v[64:65], v[26:27], v[28:29]
	v_lshl_add_u32 v23, v25, 6, s2
	v_mov_b32_e32 v67, v66
	s_mov_b32 s18, s10
	s_mov_b32 s19, s11
	buffer_store_dwordx4 v[64:67], v23, s[16:19], 0 offen sc1
